# differential-attention unit prologue: compiler-inserted vmcnt(0) drain between the LDS-DMA issues and the Q loads removed; plus gathered-GEMM index loads, residual epilogue, MLA loop reorder
# speedup vs baseline: 1.0119x; 1.0063x over previous
; #define ATT_DMA_K(t, sl) do { glds16(ksrc + (size_t)(t) * 64 * kpitch, (unsigned)__builtin_amdgcn_readfirstlane(kdst + (sl) * KSLOT)); \
;         if constexpr (DQK == 96) glds16(krsrc + (size_t)(t) * 64 * 32, (unsigned)__builtin_amdgcn_readfirstlane(krdst + (sl) * KSLOT)); } while (0)
; #define ATT_DMA_V(t, sl) do { glds16(vsrc + (size_t)(t) * 64, (unsigned)__builtin_amdgcn_readfirstlane(vdst + (sl) * VSLOT)); \
;         if constexpr (DV == 128) glds16(vsrc + (size_t)64 * NR + (size_t)(t) * 64, (unsigned)__builtin_amdgcn_readfirstlane(vdst + (sl) * VSLOT + 8192)); } while (0)
; template <int DQK, int DV, bool LEAD> ...
;     ...
;     ATT_DMA_K(0, 0); ATT_DMA_V(0, 0); ATT_DMA_K(1, 1); ATT_DMA_K(2, 2);
;     bf16x8 qf[NQB * NDS];
;     {
;       const float c2 = (DQK == 64) ? C2_EVEN : C2_ODD; const bool lat = tq0 >= 0;
; #pragma unroll
;       for (int qb = 0; qb < NQB; ++qb) {
;           const bf16_t* qp = Q + (size_t)(qrow0 + qoff + qb * 16 + q16) * qpitch + g4 * 8;
;           bf16x8 raw[NDS];
; #pragma unroll
;           for (int ds = 0; ds < NDS; ++ds) raw[ds] = *(const bf16x8*)(qp + ds * 32);
;           float x[NDS][8];
; #pragma unroll
;           for (int ds = 0; ds < NDS; ++ds)
; #pragma unroll
;               for (int j = 0; j < 8; ++j) x[ds][j] = __uint_as_float(((unsigned)(unsigned short)raw[ds][j]) << 16);
;           const int tq = tq0 + qoff + qb * 16 + q16, prow = (tq >> 6) & 127, pcol = tq & 63;
;           float sn = 0.f;
; #pragma unroll
;           for (int ds = 0; ds < 2; ++ds)
; #pragma unroll
;               for (int j = 0; j < 8; ++j) sn += x[ds][j] * x[ds][j];
;           sn = lanes4_sum(sn);
;           const float rn = rsqrtf(sn * (1.f / 64.f) + EPS);
; #pragma unroll
;           for (int ds = 0; ds < 2; ++ds)
; #pragma unroll
;               for (int j = 0; j < 8; ++j) x[ds][j] *= rn * qgain[32 * ds + 8 * g4 + j];
.LBB0_939:
	s_lshl_b32 s6, s4, 1
	s_and_b32 s6, s6, 0x180
	s_lshr_b32 s5, s4, 8
	s_lshl_b32 s7, s6, 1
	s_add_u32 s16, s18, s7
	s_addc_u32 s22, s19, 0
	s_lshl_b32 s23, s4, 2
	s_and_b32 s23, s23, 0x80
	s_add_u32 s36, s16, s23
	s_addc_u32 s37, s22, 0
	s_add_u32 s7, s15, s7
	s_addc_u32 s16, s17, 0
	s_add_u32 s40, s7, s23
	s_addc_u32 s41, s16, 0
	s_mul_i32 s6, s6, 0x21000
	s_add_u32 s44, s10, s6
	s_addc_u32 s45, s11, 0
	s_lshl_b32 s6, s4, 3
	s_and_b32 s6, s6, 0x700
	s_add_u32 s26, s3, s6
	s_mov_b64 s[6:7], s[0:1]
	s_load_dwordx2 s[6:7], s[6:7], 0x48
	s_addc_u32 s27, s14, 0
	s_lshl_b32 s25, s4, 8
	s_mul_i32 s46, s5, 0x2100
	s_and_b32 s4, s25, 0x1f00
	s_add_i32 s30, s46, s4
	s_lshl_b64 s[22:23], s[20:21], 2
	s_waitcnt lgkmcnt(0)
	s_add_u32 s28, s6, s22
	s_addc_u32 s29, s7, s23
	v_readfirstlane_b32 s4, v0
	s_cmpk_gt_u32 s4, 0xff
	s_mov_b64 s[4:5], -1
	s_cbranch_scc0 .LBB0_946
	v_mov_b32_e32 v79, v0
	s_ashr_i32 s47, s46, 31
	v_readfirstlane_b32 s4, v79
	s_ashr_i32 s42, s4, 6
	v_bfe_u32 v1, v79, 3, 3
	v_lshl_or_b32 v6, s42, 3, v1
	s_lshl_b32 s5, s42, 1
	s_lshr_b32 s4, s4, 5
	v_ashrrev_i32_e32 v2, 1, v6
	s_and_b32 s5, s5, 2
	s_and_b32 s4, s4, 4
	v_and_b32_e32 v203, 7, v79
	v_and_b32_e32 v3, 1, v2
	s_or_b32 s4, s5, s4
	v_bitop3_b32 v7, s4, v203, v3 bitop3:0x36
	v_xor_b32_e32 v8, v2, v79
	v_add_u32_e32 v4, s46, v6
	v_mov_b64_e32 v[2:3], s[40:41]
	v_mad_i64_i32 v[2:3], s[4:5], v4, s92, v[2:3]
	v_mov_b64_e32 v[4:5], s[44:45]
	v_lshlrev_b32_e32 v194, 4, v7
	s_lshl_b32 s43, s42, 10
	v_mad_i64_i32 v[4:5], s[4:5], v6, s91, v[4:5]
	v_lshl_add_u64 v[204:205], v[2:3], 0, v[194:195]
	v_lshlrev_b32_e32 v2, 4, v8
	s_add_i32 s43, s43, 0
	v_lshl_add_u64 v[4:5], s[46:47], 1, v[4:5]
	v_and_b32_e32 v194, 0x70, v2
	s_mov_b32 s4, m0
	s_mov_b32 m0, s43
	s_nop 0
	global_load_lds_dwordx4 v[204:205], off
	s_mov_b32 m0, s4
	v_lshl_add_u64 v[206:207], v[4:5], 0, v[194:195]
	s_add_i32 s16, s43, 0x9000
	s_mov_b32 s4, m0
	s_mov_b32 m0, s16
	s_nop 0
	global_load_lds_dwordx4 v[206:207], off
	s_mov_b32 m0, s4
	s_mov_b64 s[4:5], 0x840000
	v_lshl_add_u64 v[208:209], v[206:207], 0, s[4:5]
	s_add_i32 s4, s16, 0x2000
	s_mov_b32 s5, m0
	s_mov_b32 m0, s4
	s_nop 0
	global_load_lds_dwordx4 v[208:209], off
	s_mov_b32 m0, s5
	s_mov_b64 s[4:5], 0x38000
	v_lshl_add_u64 v[2:3], v[204:205], 0, s[4:5]
	s_add_i32 s4, s43, 0x2000
	s_mov_b32 s5, m0
	s_mov_b32 m0, s4
	s_nop 0
	global_load_lds_dwordx4 v[2:3], off
	s_mov_b32 m0, s5
	s_lshl_b32 s6, s42, 5
	s_mov_b64 s[4:5], 0x70000
	v_and_b32_e32 v78, 15, v79
	v_lshl_add_u64 v[2:3], v[204:205], 0, s[4:5]
	s_add_i32 s31, s6, s30
	v_and_b32_e32 v194, 48, v79
	s_add_i32 s4, s43, 0x4000
	s_mov_b32 s5, m0
	s_mov_b32 m0, s4
	s_nop 0
	global_load_lds_dwordx4 v[2:3], off
	s_mov_b32 m0, s5
	v_or_b32_e32 v4, s31, v78
	v_lshl_add_u64 v[2:3], s[36:37], 0, v[194:195]
	v_lshrrev_b32_e32 v38, 1, v79
	v_or_b32_e32 v5, s6, v78
	v_mad_i64_i32 v[26:27], s[4:5], v4, s92, v[2:3]
	v_and_b32_e32 v28, 8, v38
	v_lshlrev_b32_e32 v5, 4, v5
	s_movk_i32 s4, 0x2f0
	v_or_b32_e32 v4, 16, v4
	v_and_or_b32 v5, v5, s4, v28
	v_mad_i64_i32 v[30:31], s[4:5], v4, s92, v[2:3]
	s_add_i32 s6, s6, s25
	s_lshr_b32 s4, s6, 2
	v_lshlrev_b32_e32 v22, 3, v5
	s_and_b32 s4, s4, 0x7f0
	global_load_dwordx4 v[50:53], v[26:27], off offset:64
	global_load_dwordx4 v[60:63], v22, s[8:9] offset:48
	global_load_dwordx4 v[70:73], v[30:31], off offset:64
	global_load_dwordx4 v[6:9], v22, s[8:9] offset:2096
	global_load_dwordx4 v[54:57], v22, s[8:9] offset:32
	global_load_dwordx4 v[14:17], v22, s[8:9] offset:2080
	global_load_dwordx4 v[2:5], v22, s[8:9] offset:16
	global_load_dwordx4 v[18:21], v22, s[8:9] offset:2064
	global_load_dwordx4 v[10:13], v22, s[8:9]
	s_nop 0
	global_load_dwordx4 v[22:25], v22, s[8:9] offset:2048
	s_nop 0
	global_load_dwordx4 v[82:85], v[26:27], off
	v_or_b32_e32 v26, s4, v28
	v_lshlrev_b32_e32 v39, 3, v26
	global_load_dwordx4 v[26:29], v39, s[8:9] offset:48
	global_load_dwordx4 v[86:89], v[30:31], off
	s_nop 0
	global_load_dwordx4 v[30:33], v39, s[8:9] offset:32
	global_load_dwordx4 v[34:37], v39, s[8:9] offset:16
	v_bfe_u32 v214, v79, 4, 2
	v_lshlrev_b32_e32 v215, 1, v79
	v_and_b32_e32 v40, 3, v79
	v_and_or_b32 v40, v215, 24, v40
	v_bitop3_b32 v38, v214, v38, 7 bitop3:0x78
	v_lshlrev_b32_e32 v59, 5, v214
	v_lshl_add_u32 v81, v40, 7, 0
	v_lshlrev_b32_e32 v80, 4, v38
	global_load_dwordx4 v[38:41], v39, s[8:9]
	s_nop 0
	global_load_dwordx4 v[42:45], v59, s[28:29] offset:144
	global_load_dwordx4 v[46:49], v59, s[28:29] offset:128
	v_and_b32_e32 v58, 63, v79
	v_cmp_gt_u32_e32 vcc, 32, v58
	s_mov_b32 s4, 0x3c800000
	v_add_u32_e32 v194, v81, v80
	v_lshlrev_b32_e32 v217, 7, v78
	s_mov_b32 s47, 1
	s_mov_b32 s48, 2
	v_or_b32_e32 v216, 4, v214
	s_waitcnt vmcnt(15)
	v_and_b32_e32 v65, 0xffff0000, v73
	v_lshlrev_b32_e32 v64, 16, v73
	v_and_b32_e32 v67, 0xffff0000, v72
	v_lshlrev_b32_e32 v66, 16, v72
	s_waitcnt vmcnt(13)
	v_cndmask_b32_e64 v95, v57, -v57, vcc
	v_cndmask_b32_e64 v94, v55, -v55, vcc
	v_and_b32_e32 v91, 0xffff0000, v53
	v_lshlrev_b32_e32 v90, 16, v53
	v_and_b32_e32 v93, 0xffff0000, v52
	s_waitcnt vmcnt(5)
; template <int DQK, int DV, bool LEAD> ...
;     ...
;           for (int ds = 0; ds < NDS; ++ds) raw[ds] = *(const bf16x8*)(qp + ds * 32);
;           float x[NDS][8];
; #pragma unroll
;           for (int ds = 0; ds < NDS; ++ds)
; #pragma unroll
;               for (int j = 0; j < 8; ++j) x[ds][j] = __uint_as_float(((unsigned)(unsigned short)raw[ds][j]) << 16);
;           const int tq = tq0 + qoff + qb * 16 + q16, prow = (tq >> 6) & 127, pcol = tq & 63;
;           float sn = 0.f;
; #pragma unroll
;           for (int ds = 0; ds < 2; ++ds)
; #pragma unroll
;               for (int j = 0; j < 8; ++j) sn += x[ds][j] * x[ds][j];
;           sn = lanes4_sum(sn);
;           const float rn = rsqrtf(sn * (1.f / 64.f) + EPS);
; #pragma unroll
;           for (int ds = 0; ds < 2; ++ds)
; #pragma unroll
;               for (int j = 0; j < 8; ++j) x[ds][j] *= rn * qgain[32 * ds + 8 * g4 + j];
;           if constexpr (DQK == 64) {
; #pragma unroll
;               for (int ds = 0; ds < 2; ++ds)
; #pragma unroll
;                   for (int j = 0; j < 8; ++j) {
;                       auto rr = __builtin_amdgcn_permlane32_swap(__float_as_uint(x[ds][j]), __float_as_uint(x[ds][j]), false, false);
;                       const float other = hi ? __uint_as_float(rr[0]) : __uint_as_float(rr[1]);
;                       float cc = 1.f, sg = 0.f;
;                       if (lat) { const f32x2 cs = rope[(ds ? pcol : prow) * 16 + 8 * (g4 & 1) + j]; cc = cs.x; sg = hi ? cs.y : -cs.y; }
;                       x[ds][j] = x[ds][j] * cc + other * sg; }
	v_and_b32_e32 v73, 0xffff0000, v89
	v_lshlrev_b32_e32 v72, 16, v89
	v_and_b32_e32 v75, 0xffff0000, v88
	v_lshlrev_b32_e32 v74, 16, v88
	v_and_b32_e32 v89, 0xffff0000, v83
	v_lshlrev_b32_e32 v88, 16, v83
	v_and_b32_e32 v83, 0xffff0000, v82
	v_lshlrev_b32_e32 v92, 16, v52
	v_mov_b32_e32 v55, v56
	v_and_b32_e32 v97, 0xffff0000, v51
	v_lshlrev_b32_e32 v96, 16, v51
	v_cndmask_b32_e64 v98, v3, -v3, vcc
	v_mov_b32_e32 v3, v4
	v_and_b32_e32 v101, 0xffff0000, v50
	v_lshlrev_b32_e32 v100, 16, v50
	global_load_dwordx4 v[50:53], v59, s[28:29] offset:16
	s_nop 0
	global_load_dwordx4 v[56:59], v59, s[28:29]
	v_lshlrev_b32_e32 v82, 16, v82
	v_mul_f32_e32 v4, v83, v83
	v_cndmask_b32_e64 v99, v5, -v5, vcc
	v_pk_fma_f32 v[4:5], v[82:83], v[82:83], v[4:5] op_sel_hi:[1,1,0]
	v_mul_f32_e32 v104, v89, v89
	v_pk_fma_f32 v[4:5], v[88:89], v[88:89], v[4:5]
	v_cndmask_b32_e64 v103, v13, -v13, vcc
	v_cndmask_b32_e64 v102, v11, -v11, vcc
	v_mov_b32_e32 v11, v12
	v_and_b32_e32 v13, 0xffff0000, v85
	v_lshlrev_b32_e32 v12, 16, v85
	v_and_b32_e32 v85, 0xffff0000, v84
	v_lshlrev_b32_e32 v84, 16, v84
	v_pk_add_f32 v[4:5], v[104:105], v[4:5] op_sel_hi:[0,1]
	v_pk_fma_f32 v[4:5], v[84:85], v[84:85], v[4:5]
	v_mul_f32_e32 v104, v85, v85
	v_pk_add_f32 v[4:5], v[104:105], v[4:5] op_sel_hi:[0,1]
	v_pk_fma_f32 v[4:5], v[12:13], v[12:13], v[4:5]
	v_mul_f32_e32 v104, v13, v13
	v_pk_add_f32 v[4:5], v[104:105], v[4:5] op_sel_hi:[0,1]
	v_pk_fma_f32 v[4:5], v[100:101], v[100:101], v[4:5]
	v_mul_f32_e32 v104, v101, v101
	v_pk_add_f32 v[4:5], v[104:105], v[4:5] op_sel_hi:[0,1]
	v_pk_fma_f32 v[4:5], v[96:97], v[96:97], v[4:5]
	v_mul_f32_e32 v104, v97, v97
	v_pk_add_f32 v[4:5], v[104:105], v[4:5] op_sel_hi:[0,1]
	v_pk_fma_f32 v[4:5], v[92:93], v[92:93], v[4:5]
	v_mul_f32_e32 v104, v93, v93
	v_pk_add_f32 v[4:5], v[104:105], v[4:5] op_sel_hi:[0,1]
	v_pk_fma_f32 v[4:5], v[90:91], v[90:91], v[4:5]
	v_mul_f32_e32 v104, v91, v91
	v_pk_add_f32 v[4:5], v[104:105], v[4:5] op_sel_hi:[0,1]
	v_mov_b32_e32 v5, v4
	s_nop 1
	v_permlane16_swap_b32_e32 v4, v5
	v_add_f32_e32 v5, v4, v5
	v_cndmask_b32_e64 v77, v63, -v63, vcc
	v_cndmask_b32_e64 v76, v61, -v61, vcc
	v_mov_b32_e32 v61, v62
	v_cndmask_b32_e64 v63, v9, -v9, vcc
	v_cndmask_b32_e64 v62, v7, -v7, vcc
	v_mov_b32_e32 v7, v8
	v_cndmask_b32_e64 v9, v17, -v17, vcc
	v_cndmask_b32_e64 v8, v15, -v15, vcc
	v_mov_b32_e32 v15, v16
	v_cndmask_b32_e64 v17, v21, -v21, vcc
	v_cndmask_b32_e64 v16, v19, -v19, vcc
	v_mov_b32_e32 v19, v20
	v_cndmask_b32_e64 v21, v25, -v25, vcc
	v_cndmask_b32_e64 v20, v23, -v23, vcc
	v_mov_b32_e32 v23, v24
	v_cndmask_b32_e64 v25, v29, -v29, vcc
	v_cndmask_b32_e64 v24, v27, -v27, vcc
	v_mov_b32_e32 v27, v28
	s_waitcnt vmcnt(6)
	v_cndmask_b32_e64 v29, v33, -v33, vcc
	v_cndmask_b32_e64 v28, v31, -v31, vcc
	v_mov_b32_e32 v31, v32
	s_waitcnt vmcnt(5)
	v_cndmask_b32_e64 v33, v37, -v37, vcc
	v_cndmask_b32_e64 v32, v35, -v35, vcc
	v_mov_b32_e32 v35, v36
	v_and_b32_e32 v37, 0xffff0000, v87
	v_lshlrev_b32_e32 v36, 16, v87
	v_mov_b32_e32 v87, v5
	v_and_b32_e32 v105, 0xffff0000, v86
	s_nop 0
	v_permlane32_swap_b32_e32 v5, v87
	v_lshlrev_b32_e32 v104, 16, v86
	v_mul_f32_e32 v4, v105, v105
	v_pk_fma_f32 v[106:107], v[104:105], v[104:105], v[4:5] op_sel_hi:[1,1,0]
	v_mul_f32_e32 v4, v37, v37
	v_pk_fma_f32 v[106:107], v[36:37], v[36:37], v[106:107]
	v_and_b32_e32 v69, 0xffff0000, v71
	v_pk_add_f32 v[106:107], v[4:5], v[106:107] op_sel_hi:[0,1]
	v_pk_fma_f32 v[106:107], v[74:75], v[74:75], v[106:107]
	v_mul_f32_e32 v4, v75, v75
	v_pk_add_f32 v[106:107], v[4:5], v[106:107] op_sel_hi:[0,1]
	v_pk_fma_f32 v[106:107], v[72:73], v[72:73], v[106:107]
	v_mul_f32_e32 v4, v73, v73
	v_lshlrev_b32_e32 v68, 16, v71
	v_and_b32_e32 v71, 0xffff0000, v70
	v_lshlrev_b32_e32 v70, 16, v70
	v_pk_add_f32 v[106:107], v[4:5], v[106:107] op_sel_hi:[0,1]
	v_pk_fma_f32 v[106:107], v[70:71], v[70:71], v[106:107]
	v_mul_f32_e32 v4, v71, v71
	v_pk_add_f32 v[106:107], v[4:5], v[106:107] op_sel_hi:[0,1]
	v_pk_fma_f32 v[106:107], v[68:69], v[68:69], v[106:107]
	v_mul_f32_e32 v4, v69, v69
	v_pk_add_f32 v[106:107], v[4:5], v[106:107] op_sel_hi:[0,1]
	v_pk_fma_f32 v[106:107], v[66:67], v[66:67], v[106:107]
	v_mul_f32_e32 v4, v67, v67
	v_pk_add_f32 v[106:107], v[4:5], v[106:107] op_sel_hi:[0,1]
	v_pk_fma_f32 v[106:107], v[64:65], v[64:65], v[106:107]
	v_mul_f32_e32 v4, v65, v65
	v_pk_add_f32 v[106:107], v[4:5], v[106:107] op_sel_hi:[0,1]
	v_mov_b32_e32 v4, v106
	s_nop 1
	v_permlane16_swap_b32_e32 v106, v4
	v_add_f32_e32 v4, v106, v4
	v_mov_b32_e32 v86, v4
	s_nop 1
	v_permlane32_swap_b32_e32 v4, v86
	v_pk_add_f32 v[4:5], v[4:5], v[86:87]
	s_waitcnt vmcnt(4)
	v_cndmask_b32_e64 v106, v39, -v39, vcc
	v_pk_fma_f32 v[86:87], v[4:5], s[4:5], v[196:197] op_sel_hi:[1,0,0]
	v_mov_b32_e32 v39, v40
	v_mul_f32_e32 v4, 0x4b800000, v87
	v_cmp_gt_f32_e64 s[4:5], s95, v87
	v_cndmask_b32_e64 v107, v41, -v41, vcc
	s_nop 0
	v_cndmask_b32_e64 v4, v87, v4, s[4:5]
	v_rsq_f32_e32 v4, v4
	s_nop 0
	v_mul_f32_e32 v5, 0x45800000, v4
	v_cndmask_b32_e64 v40, v4, v5, s[4:5]
	s_waitcnt vmcnt(3)
	v_pk_mul_f32 v[4:5], v[40:41], v[44:45] op_sel_hi:[0,1]
	v_pk_mul_f32 v[4:5], v[4:5], v[90:91]
	v_cmp_gt_f32_e64 s[4:5], s95, v86
	v_mov_b32_e32 v41, v4
	v_mov_b32_e32 v87, v4
	v_mov_b32_e32 v90, v5
	v_mov_b32_e32 v91, v5
	v_permlane32_swap_b32_e32 v41, v87
	s_nop 0
	v_permlane32_swap_b32_e32 v90, v91
	v_cndmask_b32_e32 v91, v90, v91, vcc
	v_cndmask_b32_e32 v90, v41, v87, vcc
	v_pk_mul_f32 v[76:77], v[76:77], v[90:91]
	s_nop 0
	v_pk_fma_f32 v[4:5], v[4:5], v[60:61], v[76:77]
	v_pk_mul_f32 v[60:61], v[40:41], v[42:43] op_sel_hi:[0,1]
	v_pk_mul_f32 v[4:5], v[4:5], s[94:95] op_sel_hi:[1,0]
	v_pk_mul_f32 v[60:61], v[60:61], v[92:93]
	v_cvt_pk_bf16_f32 v5, v4, v5
	v_mov_b32_e32 v4, v60
	v_mov_b32_e32 v41, v60
	v_mov_b32_e32 v76, v61
	v_mov_b32_e32 v77, v61
	v_permlane32_swap_b32_e32 v4, v41
	s_nop 0
	v_permlane32_swap_b32_e32 v76, v77
	v_cndmask_b32_e32 v77, v76, v77, vcc
	v_cndmask_b32_e32 v76, v4, v41, vcc
	v_pk_mul_f32 v[76:77], v[94:95], v[76:77]
	s_nop 0
	v_pk_fma_f32 v[54:55], v[60:61], v[54:55], v[76:77]
	s_nop 0
	v_pk_mul_f32 v[54:55], v[54:55], s[94:95] op_sel_hi:[1,0]
	s_nop 0
	v_cvt_pk_bf16_f32 v4, v54, v55
	s_waitcnt vmcnt(2)
; __device__ __forceinline__ unsigned cvtpk(float lo, float hi) { f32x2 v = {lo, hi}; bf16x2_t b = __builtin_convertvector(v, bf16x2_t); return __builtin_bit_cast(unsigned, b); }
; template <int DQK, int DV, bool LEAD> ...
;     ...
;           sn = lanes4_sum(sn);
;           const float rn = rsqrtf(sn * (1.f / 64.f) + EPS);
; #pragma unroll
;           for (int ds = 0; ds < 2; ++ds)
; #pragma unroll
;               for (int j = 0; j < 8; ++j) x[ds][j] *= rn * qgain[32 * ds + 8 * g4 + j];
;           if constexpr (DQK == 64) {
; #pragma unroll
;               for (int ds = 0; ds < 2; ++ds)
; #pragma unroll
;                   for (int j = 0; j < 8; ++j) {
;                       auto rr = __builtin_amdgcn_permlane32_swap(__float_as_uint(x[ds][j]), __float_as_uint(x[ds][j]), false, false);
;                       const float other = hi ? __uint_as_float(rr[0]) : __uint_as_float(rr[1]);
;                       float cc = 1.f, sg = 0.f;
;                       if (lat) { const f32x2 cs = rope[(ds ? pcol : prow) * 16 + 8 * (g4 & 1) + j]; cc = cs.x; sg = hi ? cs.y : -cs.y; }
;                       x[ds][j] = x[ds][j] * cc + other * sg; }
;           } else {
;               float sr = 0.f;
; #pragma unroll
;               for (int j = 0; j < 8; ++j) sr += x[2][j] * x[2][j];
;               sr = lanes4_sum(sr);
;               const float rq = rsqrtf(sr * (1.f / 32.f) + EPS);
; #pragma unroll
;               for (int j = 0; j < 8; ++j) { const float av = x[2][j] * rq * qgain[64 + 8 * g4 + j];
;                   auto rr = __builtin_amdgcn_permlane16_swap(__float_as_uint(av), __float_as_uint(av), false, false);
;                   const float other = (g4 & 1) ? __uint_as_float(rr[0]) : __uint_as_float(rr[1]);
;                   float cc = 1.f, sg = 0.f;
;                   if (lat) { const f32x2 cs = rope[((g4 & 2) ? pcol : prow) * 8 + j]; cc = cs.x; sg = (g4 & 1) ? cs.y : -cs.y; }
;                   x[2][j] = av * cc + other * sg; }
;           }
; #pragma unroll
;           for (int ds = 0; ds < NDS; ++ds) { u32x4 w;
; #pragma unroll
;               for (int i = 0; i < 4; ++i) w[i] = cvtpk(x[ds][2 * i] * c2, x[ds][2 * i + 1] * c2);
;               qf[qb * NDS + ds] = __builtin_bit_cast(bf16x8, w); }
	v_pk_mul_f32 v[54:55], v[40:41], v[48:49] op_sel_hi:[0,1]
	v_pk_mul_f32 v[54:55], v[54:55], v[96:97]
	s_nop 0
	v_mov_b32_e32 v41, v54
	v_mov_b32_e32 v60, v54
	v_mov_b32_e32 v61, v55
	v_mov_b32_e32 v76, v55
	v_permlane32_swap_b32_e32 v41, v60
	s_nop 0
	v_permlane32_swap_b32_e32 v61, v76
	v_cndmask_b32_e32 v61, v61, v76, vcc
	v_cndmask_b32_e32 v60, v41, v60, vcc
	v_pk_mul_f32 v[60:61], v[98:99], v[60:61]
	s_nop 0
	v_pk_fma_f32 v[2:3], v[54:55], v[2:3], v[60:61]
	v_pk_mul_f32 v[54:55], v[46:47], v[40:41] op_sel_hi:[1,0]
	v_pk_mul_f32 v[2:3], v[2:3], s[94:95] op_sel_hi:[1,0]
	v_pk_mul_f32 v[54:55], v[54:55], v[100:101]
	v_cvt_pk_bf16_f32 v3, v2, v3
	v_mov_b32_e32 v2, v54
	v_mov_b32_e32 v41, v54
	v_mov_b32_e32 v60, v55
	v_mov_b32_e32 v61, v55
	v_permlane32_swap_b32_e32 v2, v41
	s_nop 0
	v_permlane32_swap_b32_e32 v60, v61
	v_cndmask_b32_e32 v61, v60, v61, vcc
	v_cndmask_b32_e32 v60, v2, v41, vcc
	v_pk_mul_f32 v[60:61], v[102:103], v[60:61]
	s_nop 0
	v_pk_fma_f32 v[10:11], v[54:55], v[10:11], v[60:61]
	s_nop 0
	v_pk_mul_f32 v[10:11], v[10:11], s[94:95] op_sel_hi:[1,0]
	s_nop 0
	v_cvt_pk_bf16_f32 v2, v10, v11
	s_waitcnt vmcnt(1)
	v_pk_mul_f32 v[10:11], v[52:53], v[40:41] op_sel_hi:[1,0]
	s_nop 0
	v_pk_mul_f32 v[10:11], v[10:11], v[12:13]
	s_nop 0
	v_mov_b32_e32 v12, v10
	v_mov_b32_e32 v41, v10
	v_mov_b32_e32 v13, v11
	v_mov_b32_e32 v54, v11
	v_permlane32_swap_b32_e32 v12, v41
	s_nop 0
	v_permlane32_swap_b32_e32 v13, v54
	v_cndmask_b32_e32 v13, v13, v54, vcc
	v_cndmask_b32_e32 v12, v12, v41, vcc
	v_pk_mul_f32 v[12:13], v[24:25], v[12:13]
	s_nop 0
	v_pk_fma_f32 v[10:11], v[10:11], v[26:27], v[12:13]
	s_nop 0
	v_pk_mul_f32 v[10:11], v[10:11], s[94:95] op_sel_hi:[1,0]
	s_nop 0
	v_cvt_pk_bf16_f32 v13, v10, v11
	v_pk_mul_f32 v[10:11], v[50:51], v[40:41] op_sel_hi:[1,0]
	s_nop 0
	v_pk_mul_f32 v[10:11], v[10:11], v[84:85]
	s_nop 0
	v_mov_b32_e32 v12, v10
	v_mov_b32_e32 v41, v10
	v_mov_b32_e32 v54, v11
	v_mov_b32_e32 v55, v11
	v_permlane32_swap_b32_e32 v12, v41
	s_nop 0
	v_permlane32_swap_b32_e32 v54, v55
	v_cndmask_b32_e32 v55, v54, v55, vcc
	v_cndmask_b32_e32 v54, v12, v41, vcc
	v_pk_mul_f32 v[54:55], v[28:29], v[54:55]
	s_nop 0
	v_pk_fma_f32 v[10:11], v[10:11], v[30:31], v[54:55]
	s_nop 0
	v_pk_mul_f32 v[10:11], v[10:11], s[94:95] op_sel_hi:[1,0]
	s_nop 0
	v_cvt_pk_bf16_f32 v12, v10, v11
	s_waitcnt vmcnt(0)
	v_pk_mul_f32 v[10:11], v[58:59], v[40:41] op_sel_hi:[1,0]
	s_nop 0
	v_pk_mul_f32 v[10:11], v[10:11], v[88:89]
	s_nop 0
	v_mov_b32_e32 v41, v10
	v_mov_b32_e32 v54, v10
	v_mov_b32_e32 v55, v11
	v_mov_b32_e32 v60, v11
	v_permlane32_swap_b32_e32 v41, v54
	s_nop 0
	v_permlane32_swap_b32_e32 v55, v60
	v_cndmask_b32_e32 v55, v55, v60, vcc
	v_cndmask_b32_e32 v54, v41, v54, vcc
	v_pk_mul_f32 v[54:55], v[32:33], v[54:55]
	v_pk_mul_f32 v[40:41], v[56:57], v[40:41] op_sel_hi:[1,0]
	v_pk_fma_f32 v[10:11], v[10:11], v[34:35], v[54:55]
	v_pk_mul_f32 v[40:41], v[40:41], v[82:83]
	v_pk_mul_f32 v[10:11], v[10:11], s[94:95] op_sel_hi:[1,0]
	v_mov_b32_e32 v54, v40
	v_cvt_pk_bf16_f32 v11, v10, v11
	v_mov_b32_e32 v10, v40
	s_nop 1
	v_permlane32_swap_b32_e32 v10, v54
	v_mov_b32_e32 v55, v41
	v_mov_b32_e32 v60, v41
	v_cndmask_b32_e32 v54, v10, v54, vcc
	v_mul_f32_e32 v10, 0x4b800000, v86
	v_permlane32_swap_b32_e32 v55, v60
	v_cndmask_b32_e64 v10, v86, v10, s[4:5]
	v_cndmask_b32_e32 v55, v55, v60, vcc
	v_rsq_f32_e32 v60, v10
	v_pk_mul_f32 v[54:55], v[106:107], v[54:55]
	s_nop 0
	v_pk_fma_f32 v[40:41], v[40:41], v[38:39], v[54:55]
	s_nop 0
	v_pk_mul_f32 v[40:41], v[40:41], s[94:95] op_sel_hi:[1,0]
	s_nop 0
	v_cvt_pk_bf16_f32 v10, v40, v41
	v_mul_f32_e32 v40, 0x45800000, v60
	v_cndmask_b32_e64 v40, v60, v40, s[4:5]
	v_pk_mul_f32 v[54:55], v[56:57], v[40:41] op_sel_hi:[1,0]
	v_pk_mul_f32 v[56:57], v[58:59], v[40:41] op_sel_hi:[1,0]
	v_pk_mul_f32 v[54:55], v[54:55], v[104:105]
	v_pk_mul_f32 v[36:37], v[56:57], v[36:37]
	v_pk_mul_f32 v[50:51], v[50:51], v[40:41] op_sel_hi:[1,0]
	v_pk_mul_f32 v[52:53], v[52:53], v[40:41] op_sel_hi:[1,0]
	v_pk_mul_f32 v[46:47], v[46:47], v[40:41] op_sel_hi:[1,0]
	v_pk_mul_f32 v[48:49], v[48:49], v[40:41] op_sel_hi:[1,0]
	v_pk_mul_f32 v[42:43], v[42:43], v[40:41] op_sel_hi:[1,0]
	v_pk_mul_f32 v[40:41], v[44:45], v[40:41] op_sel_hi:[1,0]
	v_mov_b32_e32 v44, v54
	v_mov_b32_e32 v56, v54
	v_mov_b32_e32 v45, v55
	v_mov_b32_e32 v57, v55
	v_permlane32_swap_b32_e32 v44, v56
	s_nop 0
	v_permlane32_swap_b32_e32 v45, v57
	v_cndmask_b32_e32 v45, v45, v57, vcc
	v_cndmask_b32_e32 v44, v44, v56, vcc
	v_pk_mul_f32 v[38:39], v[38:39], v[54:55]
	v_mov_b32_e32 v54, v36
	v_pk_fma_f32 v[38:39], v[106:107], v[44:45], v[38:39]
	v_mov_b32_e32 v44, v36
	v_mov_b32_e32 v45, v37
	v_mov_b32_e32 v55, v37
	v_permlane32_swap_b32_e32 v44, v54
	s_nop 0
	v_permlane32_swap_b32_e32 v45, v55
	v_pk_mul_f32 v[50:51], v[50:51], v[74:75]
	v_cndmask_b32_e32 v45, v45, v55, vcc
	v_cndmask_b32_e32 v44, v44, v54, vcc
	v_pk_mul_f32 v[34:35], v[34:35], v[36:37]
	v_mov_b32_e32 v36, v50
	v_pk_fma_f32 v[32:33], v[32:33], v[44:45], v[34:35]
	v_mov_b32_e32 v34, v50
	v_mov_b32_e32 v35, v51
	v_mov_b32_e32 v37, v51
	v_permlane32_swap_b32_e32 v34, v36
	s_nop 0
	v_permlane32_swap_b32_e32 v35, v37
	v_cndmask_b32_e32 v35, v35, v37, vcc
	v_cndmask_b32_e32 v34, v34, v36, vcc
	v_pk_mul_f32 v[52:53], v[52:53], v[72:73]
	v_pk_mul_f32 v[28:29], v[28:29], v[34:35]
	v_mov_b32_e32 v34, v52
	v_pk_fma_f32 v[28:29], v[30:31], v[50:51], v[28:29]
	v_mov_b32_e32 v30, v52
	v_mov_b32_e32 v31, v53
	v_mov_b32_e32 v35, v53
	v_permlane32_swap_b32_e32 v30, v34
	s_nop 0
	v_permlane32_swap_b32_e32 v31, v35
	v_cndmask_b32_e32 v31, v31, v35, vcc
	v_cndmask_b32_e32 v30, v30, v34, vcc
	v_pk_mul_f32 v[46:47], v[46:47], v[70:71]
; __device__ __forceinline__ unsigned cvtpk(float lo, float hi) { f32x2 v = {lo, hi}; bf16x2_t b = __builtin_convertvector(v, bf16x2_t); return __builtin_bit_cast(unsigned, b); }
; #define ATT_SB() __builtin_amdgcn_sched_barrier(0)
; #define ATT_DMA_K(t, sl) do { glds16(ksrc + (size_t)(t) * 64 * kpitch, (unsigned)__builtin_amdgcn_readfirstlane(kdst + (sl) * KSLOT)); \
;         if constexpr (DQK == 96) glds16(krsrc + (size_t)(t) * 64 * 32, (unsigned)__builtin_amdgcn_readfirstlane(krdst + (sl) * KSLOT)); } while (0)
; #define ATT_DMA_V(t, sl) do { glds16(vsrc + (size_t)(t) * 64, (unsigned)__builtin_amdgcn_readfirstlane(vdst + (sl) * VSLOT)); \
;         if constexpr (DV == 128) glds16(vsrc + (size_t)64 * NR + (size_t)(t) * 64, (unsigned)__builtin_amdgcn_readfirstlane(vdst + (sl) * VSLOT + 8192)); } while (0)
; #define ATT_KLOAD(sl) do { _Pragma("unroll") for (int kb_ = 0; kb_ < NKW; ++kb_) _Pragma("unroll") for (int ds_ = 0; ds_ < NDS; ++ds_) { \
;         if (ds_ < 2) kf[kb_ * NDS + ds_] = *(const LAS bf16x8*)(kp[ds_ & 1] + (sl) * KSLOT + (kb_ & 1) * 512 + (kb_ >> 1) * 4096); \
;         else kf[kb_ * NDS + ds_] = *(const LAS bf16x8*)(krp + (sl) * KSLOT + (kb_ & 1) * 256 + (kb_ >> 1) * 2048); } } while (0)
; template <int DQK, int DV, bool LEAD> ...
;     ...
;           for (int ds = 0; ds < NDS; ++ds) { u32x4 w;
; #pragma unroll
;               for (int i = 0; i < 4; ++i) w[i] = cvtpk(x[ds][2 * i] * c2, x[ds][2 * i + 1] * c2);
;               qf[qb * NDS + ds] = __builtin_bit_cast(bf16x8, w); }
;       }
; #pragma unroll
;       for (int d0 = 0; d0 < NQB * NDS; ++d0) asm volatile("" : "+v"(qf[d0])); }
;     wait_bar<0>();
;     bf16x8 kf[NKW * NDS], vf[NVF];
;     ATT_KLOAD(0);
;     asm volatile("s_waitcnt lgkmcnt(0)\n\ts_barrier" ::: "memory");
;     float lsum[NQB];
; #pragma unroll
;     for (int qb = 0; qb < NQB; ++qb) lsum[qb] = 0.f;
;     const f32x4 zero4 = {0.f, 0.f, 0.f, 0.f};
;     f32x4 o[NDB][NQB], c[NKW][NQB]; u32x4 pw[4];
; #pragma unroll
;     for (int i = 0; i < NDB; ++i)
; #pragma unroll
;         for (int qb = 0; qb < NQB; ++qb) o[i][qb] = zero4;
;     ATT_DMA_K(3, 0); ATT_DMA_V(1, 1);
;     ATT_QK(); ATT_SB();
;     ATT_KLOAD(1); ATT_SB();
;     if constexpr (LEAD) { ATT_EXP(); ATT_SUMPACK(); }
;     wait_bar<NDMA>();
;     int s_prev = 0, s_cur = 1, s_next = 2;
;     int one_ = 1; asm volatile("" : "+s"(one_));
	v_pk_mul_f32 v[24:25], v[24:25], v[30:31]
	v_mov_b32_e32 v30, v46
	v_pk_fma_f32 v[24:25], v[52:53], v[26:27], v[24:25]
	v_mov_b32_e32 v26, v46
	v_mov_b32_e32 v27, v47
	v_mov_b32_e32 v31, v47
	v_permlane32_swap_b32_e32 v26, v30
	s_nop 0
	v_permlane32_swap_b32_e32 v27, v31
	v_cndmask_b32_e32 v27, v27, v31, vcc
	v_cndmask_b32_e32 v26, v26, v30, vcc
	v_pk_mul_f32 v[48:49], v[48:49], v[68:69]
	v_pk_mul_f32 v[20:21], v[20:21], v[26:27]
	v_mov_b32_e32 v26, v48
	v_pk_fma_f32 v[20:21], v[46:47], v[22:23], v[20:21]
	v_mov_b32_e32 v22, v48
	v_mov_b32_e32 v23, v49
	v_mov_b32_e32 v27, v49
	v_permlane32_swap_b32_e32 v22, v26
	s_nop 0
	v_permlane32_swap_b32_e32 v23, v27
	v_cndmask_b32_e32 v23, v23, v27, vcc
	v_cndmask_b32_e32 v22, v22, v26, vcc
	v_pk_mul_f32 v[42:43], v[42:43], v[66:67]
	v_pk_mul_f32 v[16:17], v[16:17], v[22:23]
	v_mov_b32_e32 v22, v42
	v_pk_fma_f32 v[16:17], v[48:49], v[18:19], v[16:17]
	v_mov_b32_e32 v18, v42
	v_mov_b32_e32 v19, v43
	v_mov_b32_e32 v23, v43
	v_permlane32_swap_b32_e32 v18, v22
	s_nop 0
	v_permlane32_swap_b32_e32 v19, v23
	v_cndmask_b32_e32 v19, v19, v23, vcc
	v_cndmask_b32_e32 v18, v18, v22, vcc
	v_pk_mul_f32 v[40:41], v[40:41], v[64:65]
	v_pk_mul_f32 v[8:9], v[8:9], v[18:19]
	v_mov_b32_e32 v18, v40
	v_pk_fma_f32 v[8:9], v[42:43], v[14:15], v[8:9]
	v_mov_b32_e32 v14, v40
	v_mov_b32_e32 v15, v41
	v_mov_b32_e32 v19, v41
	v_permlane32_swap_b32_e32 v14, v18
	s_nop 0
	v_permlane32_swap_b32_e32 v15, v19
	v_cndmask_b32_e32 v15, v15, v19, vcc
	v_cndmask_b32_e32 v14, v14, v18, vcc
	v_pk_mul_f32 v[14:15], v[62:63], v[14:15]
	v_pk_mul_f32 v[8:9], v[8:9], s[94:95] op_sel_hi:[1,0]
	v_pk_fma_f32 v[6:7], v[40:41], v[6:7], v[14:15]
	v_pk_mul_f32 v[14:15], v[38:39], s[94:95] op_sel_hi:[1,0]
	v_pk_mul_f32 v[6:7], v[6:7], s[94:95] op_sel_hi:[1,0]
	v_cvt_pk_bf16_f32 v58, v14, v15
	v_pk_mul_f32 v[14:15], v[32:33], s[94:95] op_sel_hi:[1,0]
	v_cvt_pk_bf16_f32 v68, v8, v9
	v_cvt_pk_bf16_f32 v59, v14, v15
	v_pk_mul_f32 v[14:15], v[28:29], s[94:95] op_sel_hi:[1,0]
	v_cvt_pk_bf16_f32 v69, v6, v7
	v_cvt_pk_bf16_f32 v60, v14, v15
	v_pk_mul_f32 v[14:15], v[24:25], s[94:95] op_sel_hi:[1,0]
	v_bfe_u32 v22, v79, 1, 3
	v_cvt_pk_bf16_f32 v61, v14, v15
	v_pk_mul_f32 v[14:15], v[20:21], s[94:95] op_sel_hi:[1,0]
	v_bitop3_b32 v22, v214, v22, 4 bitop3:0x36
	v_cvt_pk_bf16_f32 v66, v14, v15
	v_pk_mul_f32 v[14:15], v[16:17], s[94:95] op_sel_hi:[1,0]
	v_lshlrev_b32_e32 v30, 4, v22
	v_cvt_pk_bf16_f32 v67, v14, v15
	s_waitcnt vmcnt(0) lgkmcnt(0)
	s_barrier
	ds_read_b128 v[6:9], v194
	ds_read_b128 v[14:17], v194 offset:512
	v_add_u32_e32 v220, v81, v30
	s_waitcnt lgkmcnt(1)
	v_mfma_f32_16x16x32_bf16 v[18:21], v[6:9], v[10:13], 0
	ds_read_b128 v[22:25], v220
	ds_read_b128 v[26:29], v220 offset:512
	v_add_u32_e32 v31, 0, v217
	v_add_u32_e32 v218, v31, v80
	v_mfma_f32_16x16x32_bf16 v[6:9], v[6:9], v[58:61], 0
	v_add_u32_e32 v219, v31, v30
	s_waitcnt lgkmcnt(1)
	v_mfma_f32_16x16x32_bf16 v[126:129], v[22:25], v[66:69], v[6:9]
	v_mfma_f32_16x16x32_bf16 v[6:9], v[14:17], v[10:13], 0
	s_waitcnt lgkmcnt(0)
	v_mfma_f32_16x16x32_bf16 v[122:125], v[26:29], v[2:5], v[6:9]
	v_mfma_f32_16x16x32_bf16 v[14:17], v[14:17], v[58:61], 0
	s_nop 4
	ds_read_b128 v[6:9], v194 offset:4096
	v_mfma_f32_16x16x32_bf16 v[138:141], v[22:25], v[2:5], v[18:21]
	v_mfma_f32_16x16x32_bf16 v[114:117], v[26:29], v[66:69], v[14:17]
	s_nop 2
	ds_read_b128 v[14:17], v220 offset:4096
	ds_read_b128 v[18:21], v194 offset:4608
	ds_read_b128 v[26:29], v220 offset:4608
	s_waitcnt lgkmcnt(0)
	s_barrier
	s_waitcnt lgkmcnt(3)
	v_mfma_f32_16x16x32_bf16 v[22:25], v[6:9], v[10:13], 0
	v_mfma_f32_16x16x32_bf16 v[6:9], v[6:9], v[58:61], 0
	s_waitcnt lgkmcnt(2)
	v_mfma_f32_16x16x32_bf16 v[130:133], v[14:17], v[2:5], v[22:25]
	s_nop 4
	v_lshl_add_u64 v[22:23], v[204:205], 0, s[96:97]
	v_mfma_f32_16x16x32_bf16 v[118:121], v[14:17], v[66:69], v[6:9]
	s_mov_b32 s4, m0
	s_mov_b32 m0, s43
	s_nop 0
	global_load_lds_dwordx4 v[22:23], off
	s_mov_b32 m0, s4
	v_lshl_add_u64 v[14:15], v[206:207], 0, s[66:67]
	s_add_i32 s4, s16, 0x4000
	s_waitcnt lgkmcnt(1)
	v_mfma_f32_16x16x32_bf16 v[6:9], v[18:21], v[10:13], 0
	s_mov_b32 s5, m0
	s_mov_b32 m0, s4
	s_nop 0
	global_load_lds_dwordx4 v[14:15], off
	s_mov_b32 m0, s5
	s_mov_b64 s[4:5], 0x840080
	v_lshl_add_u64 v[22:23], v[206:207], 0, s[4:5]
	v_mfma_f32_16x16x32_bf16 v[14:17], v[18:21], v[58:61], 0
	s_add_i32 s4, s16, 0x6000
	s_mov_b32 s5, m0
	s_mov_b32 m0, s4
	s_nop 0
	global_load_lds_dwordx4 v[22:23], off
	s_mov_b32 m0, s5
	s_mov_b32 s4, 0
	s_waitcnt lgkmcnt(0)
	v_mfma_f32_16x16x32_bf16 v[142:145], v[26:29], v[2:5], v[6:9]
	s_mov_b32 s6, s4
	s_mov_b32 s7, s4
	s_mov_b32 s5, s4
	v_mfma_f32_16x16x32_bf16 v[134:137], v[26:29], v[66:69], v[14:17]
	v_mov_b64_e32 v[8:9], s[6:7]
	v_mov_b64_e32 v[6:7], s[4:5]
	ds_read_b128 v[82:85], v194 offset:8192
	ds_read_b128 v[86:89], v194 offset:8704
	ds_read_b128 v[90:93], v220 offset:8192
	ds_read_b128 v[94:97], v220 offset:8704
	ds_read_b128 v[98:101], v194 offset:12288
	ds_read_b128 v[102:105], v194 offset:12800
	ds_read_b128 v[106:109], v220 offset:12288
	ds_read_b128 v[110:113], v220 offset:12800
	s_waitcnt vmcnt(3) lgkmcnt(0)
	s_barrier
	s_mov_b32 s5, 1
	v_mov_b32_e32 v42, 0
	s_cmp_lg_u32 s5, 0
	v_mov_b64_e32 v[16:17], v[8:9]
	v_mov_b64_e32 v[20:21], v[8:9]
	v_mov_b64_e32 v[24:25], v[8:9]
	v_mov_b64_e32 v[28:29], v[8:9]
	v_mov_b64_e32 v[32:33], v[8:9]
	v_mov_b64_e32 v[36:37], v[8:9]
	v_mov_b64_e32 v[40:41], v[8:9]
	s_cselect_b64 s[6:7], -1, 0
	v_mov_b64_e32 v[14:15], v[6:7]
	v_mov_b64_e32 v[18:19], v[6:7]
	v_mov_b64_e32 v[22:23], v[6:7]
	v_mov_b64_e32 v[26:27], v[6:7]
	v_mov_b64_e32 v[30:31], v[6:7]
	v_mov_b64_e32 v[34:35], v[6:7]
	v_mov_b64_e32 v[38:39], v[6:7]
	s_mov_b32 s38, 2
	v_mov_b32_e32 v43, v42
	v_mov_b32_e32 v44, v42
	v_mov_b32_e32 v45, v42
	v_mov_b32_e32 v46, v42
	v_mov_b32_e32 v47, v42
	v_mov_b32_e32 v48, v42
	v_mov_b32_e32 v49, v42
	v_mov_b32_e32 v50, v42
	v_mov_b32_e32 v51, v42
	v_mov_b32_e32 v52, v42
	v_mov_b32_e32 v53, v42
	v_mov_b32_e32 v54, v42
	v_mov_b32_e32 v55, v42
	v_mov_b32_e32 v56, v42
	v_mov_b32_e32 v57, v42
	v_mov_b32_e32 v62, v42
	v_mov_b32_e32 v63, v42
	v_mov_b32_e32 v64, v42
	v_mov_b32_e32 v65, v42
	v_mov_b32_e32 v70, v42
	v_mov_b32_e32 v71, v42
	v_mov_b32_e32 v72, v42
	v_mov_b32_e32 v73, v42
	v_mov_b32_e32 v74, v42
	v_mov_b32_e32 v75, v42
	v_mov_b32_e32 v76, v42
	v_mov_b32_e32 v77, v42
	v_mov_b32_e32 v78, v42
	v_mov_b32_e32 v79, v42
	v_mov_b32_e32 v80, v42
	v_mov_b32_e32 v81, v42
	v_mov_b32_e32 v210, v42
	v_mov_b32_e32 v211, v42

; #define ATT_DMA_K(t, sl) do { glds16(ksrc + (size_t)(t) * 64 * kpitch, (unsigned)__builtin_amdgcn_readfirstlane(kdst + (sl) * KSLOT)); \
;         if constexpr (DQK == 96) glds16(krsrc + (size_t)(t) * 64 * 32, (unsigned)__builtin_amdgcn_readfirstlane(krdst + (sl) * KSLOT)); } while (0)
; #define ATT_DMA_V(t, sl) do { glds16(vsrc + (size_t)(t) * 64, (unsigned)__builtin_amdgcn_readfirstlane(vdst + (sl) * VSLOT)); \
;         if constexpr (DV == 128) glds16(vsrc + (size_t)64 * NR + (size_t)(t) * 64, (unsigned)__builtin_amdgcn_readfirstlane(vdst + (sl) * VSLOT + 8192)); } while (0)
; template <int DQK, int DV, bool LEAD> ...
;     ...
;     ATT_DMA_K(0, 0); ATT_DMA_V(0, 0); ATT_DMA_K(1, 1); ATT_DMA_K(2, 2);
;     bf16x8 qf[NQB * NDS];
;     {
;       const float c2 = (DQK == 64) ? C2_EVEN : C2_ODD; const bool lat = tq0 >= 0;
; #pragma unroll
;       for (int qb = 0; qb < NQB; ++qb) {
;           const bf16_t* qp = Q + (size_t)(qrow0 + qoff + qb * 16 + q16) * qpitch + g4 * 8;
;           bf16x8 raw[NDS];
; #pragma unroll
;           for (int ds = 0; ds < NDS; ++ds) raw[ds] = *(const bf16x8*)(qp + ds * 32);
;           float x[NDS][8];
; #pragma unroll
;           for (int ds = 0; ds < NDS; ++ds)
; #pragma unroll
;               for (int j = 0; j < 8; ++j) x[ds][j] = __uint_as_float(((unsigned)(unsigned short)raw[ds][j]) << 16);
;           const int tq = tq0 + qoff + qb * 16 + q16, prow = (tq >> 6) & 127, pcol = tq & 63;
;           float sn = 0.f;
; #pragma unroll
;           for (int ds = 0; ds < 2; ++ds)
; #pragma unroll
;               for (int j = 0; j < 8; ++j) sn += x[ds][j] * x[ds][j];
;           sn = lanes4_sum(sn);
;           const float rn = rsqrtf(sn * (1.f / 64.f) + EPS);
; #pragma unroll
;           for (int ds = 0; ds < 2; ++ds)
; #pragma unroll
;               for (int j = 0; j < 8; ++j) x[ds][j] *= rn * qgain[32 * ds + 8 * g4 + j];
.LBB0_946:
	s_and_b64 vcc, exec, s[4:5]
	s_cbranch_vccz .LBB0_938
	v_mov_b32_e32 v79, v0
	s_ashr_i32 s47, s46, 31
	v_readfirstlane_b32 s4, v79
	s_ashr_i32 s7, s4, 6
	v_bfe_u32 v1, v79, 3, 3
	v_lshl_or_b32 v6, s7, 3, v1
	s_lshl_b32 s5, s7, 1
	s_lshr_b32 s4, s4, 5
	v_ashrrev_i32_e32 v2, 1, v6
	s_and_b32 s5, s5, 2
	s_and_b32 s4, s4, 4
	v_and_b32_e32 v170, 7, v79
	v_and_b32_e32 v3, 1, v2
	s_or_b32 s4, s5, s4
	v_bitop3_b32 v7, s4, v170, v3 bitop3:0x36
	v_xor_b32_e32 v8, v2, v79
	v_add_u32_e32 v4, s46, v6
	s_lshl_b32 s4, s7, 10
	v_mov_b64_e32 v[2:3], s[40:41]
	s_add_i32 s31, s4, 0
	v_mad_i64_i32 v[2:3], s[4:5], v4, s92, v[2:3]
	v_mov_b64_e32 v[4:5], s[44:45]
	v_lshlrev_b32_e32 v194, 4, v7
	v_mad_i64_i32 v[4:5], s[4:5], v6, s91, v[4:5]
	v_lshl_add_u64 v[162:163], v[2:3], 0, v[194:195]
	v_lshlrev_b32_e32 v2, 4, v8
	v_lshl_add_u64 v[4:5], s[46:47], 1, v[4:5]
	v_and_b32_e32 v194, 0x70, v2
	s_mov_b32 s4, m0
	s_mov_b32 m0, s31
	s_nop 0
	global_load_lds_dwordx4 v[162:163], off
	s_mov_b32 m0, s4
	v_lshl_add_u64 v[164:165], v[4:5], 0, v[194:195]
	s_add_i32 s40, s31, 0x9000
	s_mov_b32 s4, m0
	s_mov_b32 m0, s40
	s_nop 0
	global_load_lds_dwordx4 v[164:165], off
	s_mov_b32 m0, s4
	s_mov_b64 s[4:5], 0x840000
	v_lshl_add_u64 v[166:167], v[164:165], 0, s[4:5]
	s_add_i32 s4, s40, 0x2000
	s_mov_b32 s5, m0
	s_mov_b32 m0, s4
	s_nop 0
	global_load_lds_dwordx4 v[166:167], off
	s_mov_b32 m0, s5
	s_mov_b64 s[4:5], 0x38000
	v_lshl_add_u64 v[2:3], v[162:163], 0, s[4:5]
	s_add_i32 s4, s31, 0x2000
	s_mov_b32 s5, m0
	s_mov_b32 m0, s4
	s_nop 0
	global_load_lds_dwordx4 v[2:3], off
	s_mov_b32 m0, s5
	s_lshl_b32 s16, s7, 5
	s_mov_b64 s[4:5], 0x70000
	v_and_b32_e32 v78, 15, v79
	v_lshl_add_u64 v[2:3], v[162:163], 0, s[4:5]
	s_add_i32 s6, s16, s30
	v_and_b32_e32 v194, 48, v79
	s_add_i32 s4, s31, 0x4000
	s_mov_b32 s5, m0
	s_mov_b32 m0, s4
	s_nop 0
	global_load_lds_dwordx4 v[2:3], off
	s_mov_b32 m0, s5
	v_or_b32_e32 v4, s6, v78
	v_lshl_add_u64 v[2:3], s[36:37], 0, v[194:195]
	v_lshrrev_b32_e32 v38, 1, v79
	v_or_b32_e32 v5, s16, v78
	v_mad_i64_i32 v[26:27], s[4:5], v4, s92, v[2:3]
	v_and_b32_e32 v28, 8, v38
	v_lshlrev_b32_e32 v5, 4, v5
	s_movk_i32 s4, 0x2f0
	v_or_b32_e32 v4, 16, v4
	v_and_or_b32 v5, v5, s4, v28
	v_mad_i64_i32 v[30:31], s[4:5], v4, s92, v[2:3]
	s_add_i32 s16, s16, s25
	s_lshr_b32 s4, s16, 2
	v_lshlrev_b32_e32 v22, 3, v5
	s_and_b32 s4, s4, 0x7f0
	global_load_dwordx4 v[50:53], v[26:27], off offset:64
	global_load_dwordx4 v[60:63], v22, s[8:9] offset:48
	global_load_dwordx4 v[70:73], v[30:31], off offset:64
	global_load_dwordx4 v[10:13], v22, s[8:9] offset:2096
	global_load_dwordx4 v[54:57], v22, s[8:9] offset:32
	global_load_dwordx4 v[14:17], v22, s[8:9] offset:2080
	global_load_dwordx4 v[2:5], v22, s[8:9] offset:16
	global_load_dwordx4 v[18:21], v22, s[8:9] offset:2064
	global_load_dwordx4 v[6:9], v22, s[8:9]
	s_nop 0
	global_load_dwordx4 v[22:25], v22, s[8:9] offset:2048
	s_nop 0
	global_load_dwordx4 v[82:85], v[26:27], off
	v_or_b32_e32 v26, s4, v28
	v_lshlrev_b32_e32 v39, 3, v26
	global_load_dwordx4 v[26:29], v39, s[8:9] offset:48
	global_load_dwordx4 v[86:89], v[30:31], off
	s_nop 0
	global_load_dwordx4 v[30:33], v39, s[8:9] offset:32
	global_load_dwordx4 v[34:37], v39, s[8:9] offset:16
	v_bfe_u32 v171, v79, 4, 2
	v_lshlrev_b32_e32 v172, 1, v79
	v_and_b32_e32 v40, 3, v79
	v_and_or_b32 v40, v172, 24, v40
	v_bitop3_b32 v38, v171, v38, 7 bitop3:0x78
	v_lshlrev_b32_e32 v59, 5, v171
	v_lshl_add_u32 v81, v40, 7, 0
	v_lshlrev_b32_e32 v80, 4, v38
	global_load_dwordx4 v[38:41], v39, s[8:9]
	s_nop 0
	global_load_dwordx4 v[42:45], v59, s[28:29] offset:144
	global_load_dwordx4 v[46:49], v59, s[28:29] offset:128
	v_and_b32_e32 v58, 63, v79
	v_cmp_gt_u32_e32 vcc, 32, v58
	s_mov_b32 s4, 0x3c800000
	v_add_u32_e32 v173, v81, v80
	v_lshlrev_b32_e32 v175, 7, v78
	s_mov_b32 s25, 1
	s_mov_b32 s16, 2
	v_or_b32_e32 v174, 4, v171
	s_waitcnt vmcnt(15)
	v_and_b32_e32 v65, 0xffff0000, v73
	v_lshlrev_b32_e32 v64, 16, v73
	v_and_b32_e32 v67, 0xffff0000, v72
	v_lshlrev_b32_e32 v66, 16, v72
	s_waitcnt vmcnt(13)
	v_cndmask_b32_e64 v95, v57, -v57, vcc
	v_cndmask_b32_e64 v94, v55, -v55, vcc
	v_and_b32_e32 v91, 0xffff0000, v53
	v_lshlrev_b32_e32 v90, 16, v53
	v_and_b32_e32 v93, 0xffff0000, v52
	s_waitcnt vmcnt(5)
	v_and_b32_e32 v73, 0xffff0000, v89
	v_lshlrev_b32_e32 v72, 16, v89
	v_and_b32_e32 v75, 0xffff0000, v88
	v_lshlrev_b32_e32 v74, 16, v88
	v_and_b32_e32 v89, 0xffff0000, v83
	v_lshlrev_b32_e32 v88, 16, v83
	v_and_b32_e32 v83, 0xffff0000, v82
	v_lshlrev_b32_e32 v92, 16, v52
	v_mov_b32_e32 v55, v56
	v_and_b32_e32 v97, 0xffff0000, v51
	v_lshlrev_b32_e32 v96, 16, v51
	v_cndmask_b32_e64 v98, v3, -v3, vcc
	v_mov_b32_e32 v3, v4
	v_and_b32_e32 v101, 0xffff0000, v50
	v_lshlrev_b32_e32 v100, 16, v50
	global_load_dwordx4 v[50:53], v59, s[28:29] offset:16
	s_nop 0
	global_load_dwordx4 v[56:59], v59, s[28:29]
	v_lshlrev_b32_e32 v82, 16, v82
	v_mul_f32_e32 v4, v83, v83
	v_cndmask_b32_e64 v99, v5, -v5, vcc
	v_pk_fma_f32 v[4:5], v[82:83], v[82:83], v[4:5] op_sel_hi:[1,1,0]
	v_mul_f32_e32 v104, v89, v89
	v_pk_fma_f32 v[4:5], v[88:89], v[88:89], v[4:5]
	v_cndmask_b32_e64 v103, v9, -v9, vcc
	v_cndmask_b32_e64 v102, v7, -v7, vcc
	v_mov_b32_e32 v7, v8
	v_and_b32_e32 v9, 0xffff0000, v85
	v_lshlrev_b32_e32 v8, 16, v85
	v_and_b32_e32 v85, 0xffff0000, v84
	v_lshlrev_b32_e32 v84, 16, v84
	v_pk_add_f32 v[4:5], v[104:105], v[4:5] op_sel_hi:[0,1]
	v_pk_fma_f32 v[4:5], v[84:85], v[84:85], v[4:5]
	v_mul_f32_e32 v104, v85, v85
	v_pk_add_f32 v[4:5], v[104:105], v[4:5] op_sel_hi:[0,1]
	v_pk_fma_f32 v[4:5], v[8:9], v[8:9], v[4:5]
	v_mul_f32_e32 v104, v9, v9
	v_pk_add_f32 v[4:5], v[104:105], v[4:5] op_sel_hi:[0,1]
	v_pk_fma_f32 v[4:5], v[100:101], v[100:101], v[4:5]
	v_mul_f32_e32 v104, v101, v101
	v_pk_add_f32 v[4:5], v[104:105], v[4:5] op_sel_hi:[0,1]
	v_pk_fma_f32 v[4:5], v[96:97], v[96:97], v[4:5]
	v_mul_f32_e32 v104, v97, v97
	v_pk_add_f32 v[4:5], v[104:105], v[4:5] op_sel_hi:[0,1]
	v_pk_fma_f32 v[4:5], v[92:93], v[92:93], v[4:5]
	v_mul_f32_e32 v104, v93, v93
	v_pk_add_f32 v[4:5], v[104:105], v[4:5] op_sel_hi:[0,1]
	v_pk_fma_f32 v[4:5], v[90:91], v[90:91], v[4:5]
	v_mul_f32_e32 v104, v91, v91
	v_pk_add_f32 v[4:5], v[104:105], v[4:5] op_sel_hi:[0,1]
	v_mov_b32_e32 v5, v4
	s_nop 1
	v_permlane16_swap_b32_e32 v4, v5
	v_add_f32_e32 v5, v4, v5
	v_cndmask_b32_e64 v77, v63, -v63, vcc
	v_cndmask_b32_e64 v76, v61, -v61, vcc
	v_mov_b32_e32 v61, v62
	v_cndmask_b32_e64 v63, v13, -v13, vcc
	v_cndmask_b32_e64 v62, v11, -v11, vcc
	v_mov_b32_e32 v11, v12
	v_cndmask_b32_e64 v13, v17, -v17, vcc
	v_cndmask_b32_e64 v12, v15, -v15, vcc
	v_mov_b32_e32 v15, v16
	v_cndmask_b32_e64 v17, v21, -v21, vcc
	v_cndmask_b32_e64 v16, v19, -v19, vcc
	v_mov_b32_e32 v19, v20
	v_cndmask_b32_e64 v21, v25, -v25, vcc
	v_cndmask_b32_e64 v20, v23, -v23, vcc
	v_mov_b32_e32 v23, v24
	v_cndmask_b32_e64 v25, v29, -v29, vcc
	v_cndmask_b32_e64 v24, v27, -v27, vcc
	v_mov_b32_e32 v27, v28
	s_waitcnt vmcnt(6)
; template <int DQK, int DV, bool LEAD> ...
;     ...
;           sn = lanes4_sum(sn);
;           const float rn = rsqrtf(sn * (1.f / 64.f) + EPS);
; #pragma unroll
;           for (int ds = 0; ds < 2; ++ds)
; #pragma unroll
;               for (int j = 0; j < 8; ++j) x[ds][j] *= rn * qgain[32 * ds + 8 * g4 + j];
;           if constexpr (DQK == 64) {
; #pragma unroll
;               for (int ds = 0; ds < 2; ++ds)
; #pragma unroll
;                   for (int j = 0; j < 8; ++j) {
;                       auto rr = __builtin_amdgcn_permlane32_swap(__float_as_uint(x[ds][j]), __float_as_uint(x[ds][j]), false, false);
;                       const float other = hi ? __uint_as_float(rr[0]) : __uint_as_float(rr[1]);
;                       float cc = 1.f, sg = 0.f;
;                       if (lat) { const f32x2 cs = rope[(ds ? pcol : prow) * 16 + 8 * (g4 & 1) + j]; cc = cs.x; sg = hi ? cs.y : -cs.y; }
;                       x[ds][j] = x[ds][j] * cc + other * sg; }
;           } else {
;               float sr = 0.f;
; #pragma unroll
;               for (int j = 0; j < 8; ++j) sr += x[2][j] * x[2][j];
;               sr = lanes4_sum(sr);
;               const float rq = rsqrtf(sr * (1.f / 32.f) + EPS);
; #pragma unroll
;               for (int j = 0; j < 8; ++j) { const float av = x[2][j] * rq * qgain[64 + 8 * g4 + j];
;                   auto rr = __builtin_amdgcn_permlane16_swap(__float_as_uint(av), __float_as_uint(av), false, false);
;                   const float other = (g4 & 1) ? __uint_as_float(rr[0]) : __uint_as_float(rr[1]);
;                   float cc = 1.f, sg = 0.f;
;                   if (lat) { const f32x2 cs = rope[((g4 & 2) ? pcol : prow) * 8 + j]; cc = cs.x; sg = (g4 & 1) ? cs.y : -cs.y; }
;                   x[2][j] = av * cc + other * sg; }
	v_cndmask_b32_e64 v29, v33, -v33, vcc
	v_cndmask_b32_e64 v28, v31, -v31, vcc
	v_mov_b32_e32 v31, v32
	s_waitcnt vmcnt(5)
	v_cndmask_b32_e64 v33, v37, -v37, vcc
	v_cndmask_b32_e64 v32, v35, -v35, vcc
	v_mov_b32_e32 v35, v36
	v_and_b32_e32 v37, 0xffff0000, v87
	v_lshlrev_b32_e32 v36, 16, v87
	v_mov_b32_e32 v87, v5
	v_and_b32_e32 v105, 0xffff0000, v86
	s_nop 0
	v_permlane32_swap_b32_e32 v5, v87
	v_lshlrev_b32_e32 v104, 16, v86
	v_mul_f32_e32 v4, v105, v105
	v_pk_fma_f32 v[106:107], v[104:105], v[104:105], v[4:5] op_sel_hi:[1,1,0]
	v_mul_f32_e32 v4, v37, v37
	v_pk_fma_f32 v[106:107], v[36:37], v[36:37], v[106:107]
	v_and_b32_e32 v69, 0xffff0000, v71
	v_pk_add_f32 v[106:107], v[4:5], v[106:107] op_sel_hi:[0,1]
	v_pk_fma_f32 v[106:107], v[74:75], v[74:75], v[106:107]
	v_mul_f32_e32 v4, v75, v75
	v_pk_add_f32 v[106:107], v[4:5], v[106:107] op_sel_hi:[0,1]
	v_pk_fma_f32 v[106:107], v[72:73], v[72:73], v[106:107]
	v_mul_f32_e32 v4, v73, v73
	v_lshlrev_b32_e32 v68, 16, v71
	v_and_b32_e32 v71, 0xffff0000, v70
	v_lshlrev_b32_e32 v70, 16, v70
	v_pk_add_f32 v[106:107], v[4:5], v[106:107] op_sel_hi:[0,1]
	v_pk_fma_f32 v[106:107], v[70:71], v[70:71], v[106:107]
	v_mul_f32_e32 v4, v71, v71
	v_pk_add_f32 v[106:107], v[4:5], v[106:107] op_sel_hi:[0,1]
	v_pk_fma_f32 v[106:107], v[68:69], v[68:69], v[106:107]
	v_mul_f32_e32 v4, v69, v69
	v_pk_add_f32 v[106:107], v[4:5], v[106:107] op_sel_hi:[0,1]
	v_pk_fma_f32 v[106:107], v[66:67], v[66:67], v[106:107]
	v_mul_f32_e32 v4, v67, v67
	v_pk_add_f32 v[106:107], v[4:5], v[106:107] op_sel_hi:[0,1]
	v_pk_fma_f32 v[106:107], v[64:65], v[64:65], v[106:107]
	v_mul_f32_e32 v4, v65, v65
	v_pk_add_f32 v[106:107], v[4:5], v[106:107] op_sel_hi:[0,1]
	v_mov_b32_e32 v4, v106
	s_nop 1
	v_permlane16_swap_b32_e32 v106, v4
	v_add_f32_e32 v4, v106, v4
	v_mov_b32_e32 v86, v4
	s_nop 1
	v_permlane32_swap_b32_e32 v4, v86
	v_pk_add_f32 v[4:5], v[4:5], v[86:87]
	s_waitcnt vmcnt(4)
	v_cndmask_b32_e64 v106, v39, -v39, vcc
	v_pk_fma_f32 v[86:87], v[4:5], s[4:5], v[196:197] op_sel_hi:[1,0,0]
	v_mov_b32_e32 v39, v40
	v_mul_f32_e32 v4, 0x4b800000, v87
	v_cmp_gt_f32_e64 s[4:5], s95, v87
	v_cndmask_b32_e64 v107, v41, -v41, vcc
	s_mov_b32 s28, 0
	v_cndmask_b32_e64 v4, v87, v4, s[4:5]
	v_rsq_f32_e32 v4, v4
	s_nop 0
	v_mul_f32_e32 v5, 0x45800000, v4
	v_cndmask_b32_e64 v40, v4, v5, s[4:5]
	s_waitcnt vmcnt(3)
	v_pk_mul_f32 v[4:5], v[40:41], v[44:45] op_sel_hi:[0,1]
	v_pk_mul_f32 v[4:5], v[4:5], v[90:91]
	v_cmp_gt_f32_e64 s[4:5], s95, v86
	v_mov_b32_e32 v41, v4
	v_mov_b32_e32 v87, v4
	v_mov_b32_e32 v90, v5
	v_mov_b32_e32 v91, v5
	v_permlane32_swap_b32_e32 v41, v87
	s_nop 0
	v_permlane32_swap_b32_e32 v90, v91
	v_cndmask_b32_e32 v91, v90, v91, vcc
	v_cndmask_b32_e32 v90, v41, v87, vcc
	v_pk_mul_f32 v[76:77], v[76:77], v[90:91]
	s_nop 0
	v_pk_fma_f32 v[4:5], v[4:5], v[60:61], v[76:77]
	v_pk_mul_f32 v[60:61], v[40:41], v[42:43] op_sel_hi:[0,1]
	v_pk_mul_f32 v[4:5], v[4:5], s[94:95] op_sel_hi:[1,0]
	v_pk_mul_f32 v[60:61], v[60:61], v[92:93]
	v_cvt_pk_bf16_f32 v5, v4, v5
	v_mov_b32_e32 v4, v60
	v_mov_b32_e32 v41, v60
	v_mov_b32_e32 v76, v61
	v_mov_b32_e32 v77, v61
	v_permlane32_swap_b32_e32 v4, v41
	s_nop 0
	v_permlane32_swap_b32_e32 v76, v77
	v_cndmask_b32_e32 v77, v76, v77, vcc
	v_cndmask_b32_e32 v76, v4, v41, vcc
	v_pk_mul_f32 v[76:77], v[94:95], v[76:77]
	s_nop 0
	v_pk_fma_f32 v[54:55], v[60:61], v[54:55], v[76:77]
	s_nop 0
	v_pk_mul_f32 v[54:55], v[54:55], s[94:95] op_sel_hi:[1,0]
	s_nop 0
	v_cvt_pk_bf16_f32 v4, v54, v55
	s_waitcnt vmcnt(2)
	v_pk_mul_f32 v[54:55], v[40:41], v[48:49] op_sel_hi:[0,1]
	v_pk_mul_f32 v[54:55], v[54:55], v[96:97]
	s_nop 0
	v_mov_b32_e32 v41, v54
	v_mov_b32_e32 v60, v54
	v_mov_b32_e32 v61, v55
	v_mov_b32_e32 v76, v55
	v_permlane32_swap_b32_e32 v41, v60
	s_nop 0
	v_permlane32_swap_b32_e32 v61, v76
	v_cndmask_b32_e32 v61, v61, v76, vcc
	v_cndmask_b32_e32 v60, v41, v60, vcc
	v_pk_mul_f32 v[60:61], v[98:99], v[60:61]
	s_nop 0
	v_pk_fma_f32 v[2:3], v[54:55], v[2:3], v[60:61]
	v_pk_mul_f32 v[54:55], v[46:47], v[40:41] op_sel_hi:[1,0]
	v_pk_mul_f32 v[2:3], v[2:3], s[94:95] op_sel_hi:[1,0]
	v_pk_mul_f32 v[54:55], v[54:55], v[100:101]
	v_cvt_pk_bf16_f32 v3, v2, v3
	v_mov_b32_e32 v2, v54
	v_mov_b32_e32 v41, v54
	v_mov_b32_e32 v60, v55
	v_mov_b32_e32 v61, v55
	v_permlane32_swap_b32_e32 v2, v41
	s_nop 0
	v_permlane32_swap_b32_e32 v60, v61
	v_cndmask_b32_e32 v61, v60, v61, vcc
	v_cndmask_b32_e32 v60, v2, v41, vcc
	v_pk_mul_f32 v[60:61], v[102:103], v[60:61]
	s_nop 0
	v_pk_fma_f32 v[6:7], v[54:55], v[6:7], v[60:61]
	s_nop 0
	v_pk_mul_f32 v[6:7], v[6:7], s[94:95] op_sel_hi:[1,0]
	s_nop 0
	v_cvt_pk_bf16_f32 v2, v6, v7
	s_waitcnt vmcnt(1)
	v_pk_mul_f32 v[6:7], v[52:53], v[40:41] op_sel_hi:[1,0]
	s_nop 0
	v_pk_mul_f32 v[6:7], v[6:7], v[8:9]
	s_nop 0
	v_mov_b32_e32 v8, v6
	v_mov_b32_e32 v41, v6
	v_mov_b32_e32 v9, v7
	v_mov_b32_e32 v54, v7
	v_permlane32_swap_b32_e32 v8, v41
	s_nop 0
	v_permlane32_swap_b32_e32 v9, v54
	v_cndmask_b32_e32 v9, v9, v54, vcc
	v_cndmask_b32_e32 v8, v8, v41, vcc
	v_pk_mul_f32 v[8:9], v[24:25], v[8:9]
	s_nop 0
	v_pk_fma_f32 v[6:7], v[6:7], v[26:27], v[8:9]
	s_nop 0
	v_pk_mul_f32 v[6:7], v[6:7], s[94:95] op_sel_hi:[1,0]
	s_nop 0
	v_cvt_pk_bf16_f32 v9, v6, v7
	v_pk_mul_f32 v[6:7], v[50:51], v[40:41] op_sel_hi:[1,0]
	s_nop 0
	v_pk_mul_f32 v[6:7], v[6:7], v[84:85]
	s_nop 0
	v_mov_b32_e32 v8, v6
	v_mov_b32_e32 v41, v6
	v_mov_b32_e32 v54, v7
	v_mov_b32_e32 v55, v7
	v_permlane32_swap_b32_e32 v8, v41
	s_nop 0
	v_permlane32_swap_b32_e32 v54, v55
	v_cndmask_b32_e32 v55, v54, v55, vcc
	v_cndmask_b32_e32 v54, v8, v41, vcc
	v_pk_mul_f32 v[54:55], v[28:29], v[54:55]
	s_nop 0
	v_pk_fma_f32 v[6:7], v[6:7], v[30:31], v[54:55]
	s_nop 0
	v_pk_mul_f32 v[6:7], v[6:7], s[94:95] op_sel_hi:[1,0]
	s_nop 0
	v_cvt_pk_bf16_f32 v8, v6, v7
	s_waitcnt vmcnt(0)
; __device__ __forceinline__ unsigned cvtpk(float lo, float hi) { f32x2 v = {lo, hi}; bf16x2_t b = __builtin_convertvector(v, bf16x2_t); return __builtin_bit_cast(unsigned, b); }
; template <int DQK, int DV, bool LEAD> ...
;     ...
;           sn = lanes4_sum(sn);
;           const float rn = rsqrtf(sn * (1.f / 64.f) + EPS);
; #pragma unroll
;           for (int ds = 0; ds < 2; ++ds)
; #pragma unroll
;               for (int j = 0; j < 8; ++j) x[ds][j] *= rn * qgain[32 * ds + 8 * g4 + j];
;           if constexpr (DQK == 64) {
; #pragma unroll
;               for (int ds = 0; ds < 2; ++ds)
; #pragma unroll
;                   for (int j = 0; j < 8; ++j) {
;                       auto rr = __builtin_amdgcn_permlane32_swap(__float_as_uint(x[ds][j]), __float_as_uint(x[ds][j]), false, false);
;                       const float other = hi ? __uint_as_float(rr[0]) : __uint_as_float(rr[1]);
;                       float cc = 1.f, sg = 0.f;
;                       if (lat) { const f32x2 cs = rope[(ds ? pcol : prow) * 16 + 8 * (g4 & 1) + j]; cc = cs.x; sg = hi ? cs.y : -cs.y; }
;                       x[ds][j] = x[ds][j] * cc + other * sg; }
;           } else {
;               float sr = 0.f;
; #pragma unroll
;               for (int j = 0; j < 8; ++j) sr += x[2][j] * x[2][j];
;               sr = lanes4_sum(sr);
;               const float rq = rsqrtf(sr * (1.f / 32.f) + EPS);
; #pragma unroll
;               for (int j = 0; j < 8; ++j) { const float av = x[2][j] * rq * qgain[64 + 8 * g4 + j];
;                   auto rr = __builtin_amdgcn_permlane16_swap(__float_as_uint(av), __float_as_uint(av), false, false);
;                   const float other = (g4 & 1) ? __uint_as_float(rr[0]) : __uint_as_float(rr[1]);
;                   float cc = 1.f, sg = 0.f;
;                   if (lat) { const f32x2 cs = rope[((g4 & 2) ? pcol : prow) * 8 + j]; cc = cs.x; sg = (g4 & 1) ? cs.y : -cs.y; }
;                   x[2][j] = av * cc + other * sg; }
;           }
; #pragma unroll
;           for (int ds = 0; ds < NDS; ++ds) { u32x4 w;
; #pragma unroll
;               for (int i = 0; i < 4; ++i) w[i] = cvtpk(x[ds][2 * i] * c2, x[ds][2 * i + 1] * c2);
;               qf[qb * NDS + ds] = __builtin_bit_cast(bf16x8, w); }
	v_pk_mul_f32 v[6:7], v[58:59], v[40:41] op_sel_hi:[1,0]
	s_nop 0
	v_pk_mul_f32 v[6:7], v[6:7], v[88:89]
	s_nop 0
	v_mov_b32_e32 v41, v6
	v_mov_b32_e32 v54, v6
	v_mov_b32_e32 v55, v7
	v_mov_b32_e32 v60, v7
	v_permlane32_swap_b32_e32 v41, v54
	s_nop 0
	v_permlane32_swap_b32_e32 v55, v60
	v_cndmask_b32_e32 v55, v55, v60, vcc
	v_cndmask_b32_e32 v54, v41, v54, vcc
	v_pk_mul_f32 v[54:55], v[32:33], v[54:55]
	v_pk_mul_f32 v[40:41], v[56:57], v[40:41] op_sel_hi:[1,0]
	v_pk_fma_f32 v[6:7], v[6:7], v[34:35], v[54:55]
	v_pk_mul_f32 v[40:41], v[40:41], v[82:83]
	v_pk_mul_f32 v[6:7], v[6:7], s[94:95] op_sel_hi:[1,0]
	v_mov_b32_e32 v54, v40
	v_cvt_pk_bf16_f32 v7, v6, v7
	v_mov_b32_e32 v6, v40
	s_nop 1
	v_permlane32_swap_b32_e32 v6, v54
	v_mov_b32_e32 v55, v41
	v_mov_b32_e32 v60, v41
	v_cndmask_b32_e32 v54, v6, v54, vcc
	v_mul_f32_e32 v6, 0x4b800000, v86
	v_permlane32_swap_b32_e32 v55, v60
	v_cndmask_b32_e64 v6, v86, v6, s[4:5]
	v_cndmask_b32_e32 v55, v55, v60, vcc
	v_rsq_f32_e32 v60, v6
	v_pk_mul_f32 v[54:55], v[106:107], v[54:55]
	s_nop 0
	v_pk_fma_f32 v[40:41], v[40:41], v[38:39], v[54:55]
	s_nop 0
	v_pk_mul_f32 v[40:41], v[40:41], s[94:95] op_sel_hi:[1,0]
	s_nop 0
	v_cvt_pk_bf16_f32 v6, v40, v41
	v_mul_f32_e32 v40, 0x45800000, v60
	v_cndmask_b32_e64 v40, v60, v40, s[4:5]
	v_pk_mul_f32 v[54:55], v[56:57], v[40:41] op_sel_hi:[1,0]
	v_pk_mul_f32 v[56:57], v[58:59], v[40:41] op_sel_hi:[1,0]
	v_pk_mul_f32 v[54:55], v[54:55], v[104:105]
	v_pk_mul_f32 v[36:37], v[56:57], v[36:37]
	v_pk_mul_f32 v[50:51], v[50:51], v[40:41] op_sel_hi:[1,0]
	v_pk_mul_f32 v[52:53], v[52:53], v[40:41] op_sel_hi:[1,0]
	v_pk_mul_f32 v[46:47], v[46:47], v[40:41] op_sel_hi:[1,0]
	v_pk_mul_f32 v[48:49], v[48:49], v[40:41] op_sel_hi:[1,0]
	v_pk_mul_f32 v[42:43], v[42:43], v[40:41] op_sel_hi:[1,0]
	v_pk_mul_f32 v[40:41], v[44:45], v[40:41] op_sel_hi:[1,0]
	v_mov_b32_e32 v44, v54
	v_mov_b32_e32 v56, v54
	v_mov_b32_e32 v45, v55
	v_mov_b32_e32 v57, v55
	v_permlane32_swap_b32_e32 v44, v56
	s_nop 0
	v_permlane32_swap_b32_e32 v45, v57
	v_cndmask_b32_e32 v45, v45, v57, vcc
	v_cndmask_b32_e32 v44, v44, v56, vcc
	v_pk_mul_f32 v[38:39], v[38:39], v[54:55]
	v_mov_b32_e32 v54, v36
	v_pk_fma_f32 v[38:39], v[106:107], v[44:45], v[38:39]
	v_mov_b32_e32 v44, v36
	v_mov_b32_e32 v45, v37
	v_mov_b32_e32 v55, v37
	v_permlane32_swap_b32_e32 v44, v54
	s_nop 0
	v_permlane32_swap_b32_e32 v45, v55
	v_pk_mul_f32 v[50:51], v[50:51], v[74:75]
	v_cndmask_b32_e32 v45, v45, v55, vcc
	v_cndmask_b32_e32 v44, v44, v54, vcc
	v_pk_mul_f32 v[34:35], v[34:35], v[36:37]
	v_mov_b32_e32 v36, v50
	v_pk_fma_f32 v[32:33], v[32:33], v[44:45], v[34:35]
	v_mov_b32_e32 v34, v50
	v_mov_b32_e32 v35, v51
	v_mov_b32_e32 v37, v51
	v_permlane32_swap_b32_e32 v34, v36
	s_nop 0
	v_permlane32_swap_b32_e32 v35, v37
	v_cndmask_b32_e32 v35, v35, v37, vcc
	v_cndmask_b32_e32 v34, v34, v36, vcc
	v_pk_mul_f32 v[52:53], v[52:53], v[72:73]
	v_pk_mul_f32 v[28:29], v[28:29], v[34:35]
	v_mov_b32_e32 v34, v52
	v_pk_fma_f32 v[28:29], v[30:31], v[50:51], v[28:29]
	v_mov_b32_e32 v30, v52
	v_mov_b32_e32 v31, v53
	v_mov_b32_e32 v35, v53
	v_permlane32_swap_b32_e32 v30, v34
	s_nop 0
	v_permlane32_swap_b32_e32 v31, v35
	v_cndmask_b32_e32 v31, v31, v35, vcc
	v_cndmask_b32_e32 v30, v30, v34, vcc
	v_pk_mul_f32 v[46:47], v[46:47], v[70:71]
	v_pk_mul_f32 v[24:25], v[24:25], v[30:31]
	v_mov_b32_e32 v30, v46
	v_pk_fma_f32 v[24:25], v[52:53], v[26:27], v[24:25]
	v_mov_b32_e32 v26, v46
	v_mov_b32_e32 v27, v47
	v_mov_b32_e32 v31, v47
	v_permlane32_swap_b32_e32 v26, v30
	s_nop 0
	v_permlane32_swap_b32_e32 v27, v31
	v_cndmask_b32_e32 v27, v27, v31, vcc
	v_cndmask_b32_e32 v26, v26, v30, vcc
	v_pk_mul_f32 v[48:49], v[48:49], v[68:69]
	v_pk_mul_f32 v[20:21], v[20:21], v[26:27]
	v_mov_b32_e32 v26, v48
	v_pk_fma_f32 v[20:21], v[46:47], v[22:23], v[20:21]
	v_mov_b32_e32 v22, v48
	v_mov_b32_e32 v23, v49
	v_mov_b32_e32 v27, v49
	v_permlane32_swap_b32_e32 v22, v26
	s_nop 0
	v_permlane32_swap_b32_e32 v23, v27
	v_cndmask_b32_e32 v23, v23, v27, vcc
	v_cndmask_b32_e32 v22, v22, v26, vcc
	v_pk_mul_f32 v[42:43], v[42:43], v[66:67]
	v_pk_mul_f32 v[16:17], v[16:17], v[22:23]
	v_mov_b32_e32 v22, v42
	v_pk_fma_f32 v[16:17], v[48:49], v[18:19], v[16:17]
	v_mov_b32_e32 v18, v42
	v_mov_b32_e32 v19, v43
	v_mov_b32_e32 v23, v43
	v_permlane32_swap_b32_e32 v18, v22
	s_nop 0
	v_permlane32_swap_b32_e32 v19, v23
	v_cndmask_b32_e32 v19, v19, v23, vcc
	v_cndmask_b32_e32 v18, v18, v22, vcc
	v_pk_mul_f32 v[40:41], v[40:41], v[64:65]
	v_pk_mul_f32 v[12:13], v[12:13], v[18:19]
	v_pk_mul_f32 v[16:17], v[16:17], s[94:95] op_sel_hi:[1,0]
	v_pk_fma_f32 v[18:19], v[42:43], v[14:15], v[12:13]
	v_mov_b32_e32 v12, v40
	v_mov_b32_e32 v14, v40
	v_mov_b32_e32 v13, v41
	v_mov_b32_e32 v15, v41
	v_permlane32_swap_b32_e32 v12, v14
	s_nop 0
	v_permlane32_swap_b32_e32 v13, v15
	v_cndmask_b32_e32 v13, v13, v15, vcc
	v_cndmask_b32_e32 v12, v12, v14, vcc
	v_pk_mul_f32 v[12:13], v[62:63], v[12:13]
	v_pk_mul_f32 v[14:15], v[24:25], s[94:95] op_sel_hi:[1,0]
	v_pk_fma_f32 v[22:23], v[40:41], v[10:11], v[12:13]
	v_pk_mul_f32 v[10:11], v[38:39], s[94:95] op_sel_hi:[1,0]
	v_pk_mul_f32 v[12:13], v[32:33], s[94:95] op_sel_hi:[1,0]
	v_cvt_pk_bf16_f32 v10, v10, v11
	v_cvt_pk_bf16_f32 v11, v12, v13
	v_pk_mul_f32 v[12:13], v[28:29], s[94:95] op_sel_hi:[1,0]
	v_bfe_u32 v30, v79, 1, 3
	v_cvt_pk_bf16_f32 v12, v12, v13
	v_cvt_pk_bf16_f32 v13, v14, v15
	v_pk_mul_f32 v[14:15], v[20:21], s[94:95] op_sel_hi:[1,0]
	v_bitop3_b32 v30, v171, v30, 4 bitop3:0x36
	v_cvt_pk_bf16_f32 v14, v14, v15
	v_cvt_pk_bf16_f32 v15, v16, v17
	v_pk_mul_f32 v[16:17], v[18:19], s[94:95] op_sel_hi:[1,0]
	v_pk_mul_f32 v[18:19], v[22:23], s[94:95] op_sel_hi:[1,0]
	v_cvt_pk_bf16_f32 v16, v16, v17
	v_cvt_pk_bf16_f32 v17, v18, v19
	s_waitcnt vmcnt(0) lgkmcnt(0)
	s_barrier
; #define ATT_SB() __builtin_amdgcn_sched_barrier(0)
; #define ATT_DMA_K(t, sl) do { glds16(ksrc + (size_t)(t) * 64 * kpitch, (unsigned)__builtin_amdgcn_readfirstlane(kdst + (sl) * KSLOT)); \
;         if constexpr (DQK == 96) glds16(krsrc + (size_t)(t) * 64 * 32, (unsigned)__builtin_amdgcn_readfirstlane(krdst + (sl) * KSLOT)); } while (0)
; #define ATT_DMA_V(t, sl) do { glds16(vsrc + (size_t)(t) * 64, (unsigned)__builtin_amdgcn_readfirstlane(vdst + (sl) * VSLOT)); \
;         if constexpr (DV == 128) glds16(vsrc + (size_t)64 * NR + (size_t)(t) * 64, (unsigned)__builtin_amdgcn_readfirstlane(vdst + (sl) * VSLOT + 8192)); } while (0)
; #define ATT_KLOAD(sl) do { _Pragma("unroll") for (int kb_ = 0; kb_ < NKW; ++kb_) _Pragma("unroll") for (int ds_ = 0; ds_ < NDS; ++ds_) { \
;         if (ds_ < 2) kf[kb_ * NDS + ds_] = *(const LAS bf16x8*)(kp[ds_ & 1] + (sl) * KSLOT + (kb_ & 1) * 512 + (kb_ >> 1) * 4096); \
;         else kf[kb_ * NDS + ds_] = *(const LAS bf16x8*)(krp + (sl) * KSLOT + (kb_ & 1) * 256 + (kb_ >> 1) * 2048); } } while (0)
; #define ATT_QK() do { _Pragma("unroll") for (int kb_ = 0; kb_ < NKW; ++kb_) _Pragma("unroll") for (int ds_ = 0; ds_ < NDS; ++ds_) _Pragma("unroll") for (int qb_ = 0; qb_ < NQB; ++qb_) \
;         c[kb_][qb_] = __builtin_amdgcn_mfma_f32_16x16x32_bf16(kf[kb_ * NDS + ds_], qf[qb_ * NDS + ds_], ds_ == 0 ? zero4 : c[kb_][qb_], 0, 0, 0); } while (0)
; #define ATT_EXP() do { _Pragma("unroll") for (int kb_ = 0; kb_ < NKW; ++kb_) _Pragma("unroll") for (int qb_ = 0; qb_ < NQB; ++qb_) _Pragma("unroll") for (int i_ = 0; i_ < 4; ++i_) \
;         c[kb_][qb_][i_] = __builtin_amdgcn_exp2f(c[kb_][qb_][i_]); } while (0)
; template <int DQK, int DV, bool LEAD> ...
;     ...
;     wait_bar<0>();
;     bf16x8 kf[NKW * NDS], vf[NVF];
;     ATT_KLOAD(0);
;     asm volatile("s_waitcnt lgkmcnt(0)\n\ts_barrier" ::: "memory");
;     float lsum[NQB];
; #pragma unroll
;     for (int qb = 0; qb < NQB; ++qb) lsum[qb] = 0.f;
;     const f32x4 zero4 = {0.f, 0.f, 0.f, 0.f};
;     f32x4 o[NDB][NQB], c[NKW][NQB]; u32x4 pw[4];
; #pragma unroll
;     for (int i = 0; i < NDB; ++i)
; #pragma unroll
;         for (int qb = 0; qb < NQB; ++qb) o[i][qb] = zero4;
;     ATT_DMA_K(3, 0); ATT_DMA_V(1, 1);
;     ATT_QK(); ATT_SB();
;     ATT_KLOAD(1); ATT_SB();
;     if constexpr (LEAD) { ATT_EXP(); ATT_SUMPACK(); }
;     wait_bar<NDMA>();
;     int s_prev = 0, s_cur = 1, s_next = 2;
	ds_read_b128 v[18:21], v173
	ds_read_b128 v[22:25], v173 offset:512
	v_lshlrev_b32_e32 v54, 4, v30
	v_add_u32_e32 v176, v81, v54
	s_waitcnt lgkmcnt(1)
	v_mfma_f32_16x16x32_bf16 v[26:29], v[18:21], v[6:9], 0
	ds_read_b128 v[30:33], v176
	ds_read_b128 v[34:37], v176 offset:512
	v_add_u32_e32 v55, 0, v175
	v_add_u32_e32 v178, v55, v80
	v_mfma_f32_16x16x32_bf16 v[18:21], v[18:21], v[10:13], 0
	v_add_u32_e32 v177, v55, v54
	s_waitcnt lgkmcnt(1)
	v_mfma_f32_16x16x32_bf16 v[26:29], v[30:33], v[2:5], v[26:29]
	v_mfma_f32_16x16x32_bf16 v[18:21], v[30:33], v[14:17], v[18:21]
	v_mfma_f32_16x16x32_bf16 v[30:33], v[22:25], v[6:9], 0
	v_mfma_f32_16x16x32_bf16 v[22:25], v[22:25], v[10:13], 0
	s_waitcnt lgkmcnt(0)
	v_mfma_f32_16x16x32_bf16 v[30:33], v[34:37], v[2:5], v[30:33]
	v_mfma_f32_16x16x32_bf16 v[22:25], v[34:37], v[14:17], v[22:25]
	ds_read_b128 v[34:37], v173 offset:4096
	ds_read_b128 v[38:41], v173 offset:4608
	ds_read_b128 v[46:49], v176 offset:4096
	ds_read_b128 v[50:53], v176 offset:4608
	s_waitcnt lgkmcnt(3)
	v_mfma_f32_16x16x32_bf16 v[42:45], v[34:37], v[6:9], 0
	s_waitcnt lgkmcnt(0)
	s_barrier
	v_mfma_f32_16x16x32_bf16 v[34:37], v[34:37], v[10:13], 0
	s_waitcnt lgkmcnt(1)
	v_mfma_f32_16x16x32_bf16 v[58:61], v[46:49], v[14:17], v[34:37]
	v_mfma_f32_16x16x32_bf16 v[34:37], v[38:41], v[6:9], 0
	v_mfma_f32_16x16x32_bf16 v[38:41], v[38:41], v[10:13], 0
	v_mfma_f32_16x16x32_bf16 v[42:45], v[46:49], v[2:5], v[42:45]
	v_lshl_add_u64 v[46:47], v[162:163], 0, s[96:97]
	s_mov_b32 s4, m0
	s_mov_b32 m0, s31
	s_nop 0
	global_load_lds_dwordx4 v[46:47], off
	s_mov_b32 m0, s4
	v_lshl_add_u64 v[46:47], v[164:165], 0, s[66:67]
	s_add_i32 s4, s40, 0x4000
	s_mov_b32 s5, m0
	s_mov_b32 m0, s4
	s_nop 0
	global_load_lds_dwordx4 v[46:47], off
	s_mov_b32 m0, s5
	s_mov_b64 s[4:5], 0x840080
	s_waitcnt lgkmcnt(0)
	v_mfma_f32_16x16x32_bf16 v[74:77], v[50:53], v[2:5], v[34:37]
	v_lshl_add_u64 v[46:47], v[164:165], 0, s[4:5]
	s_add_i32 s4, s40, 0x6000
	s_mov_b32 s5, m0
	s_mov_b32 m0, s4
	s_nop 0
	global_load_lds_dwordx4 v[46:47], off
	s_mov_b32 m0, s5
	v_mfma_f32_16x16x32_bf16 v[78:81], v[50:53], v[14:17], v[38:41]
	ds_read_b128 v[34:37], v173 offset:8192
	s_nop 1
	ds_read_b128 v[38:41], v173 offset:8704
	ds_read_b128 v[46:49], v176 offset:8192
	ds_read_b128 v[50:53], v176 offset:8704
	ds_read_b128 v[54:57], v173 offset:12288
	ds_read_b128 v[62:65], v173 offset:12800
	ds_read_b128 v[66:69], v176 offset:12288
	ds_read_b128 v[70:73], v176 offset:12800
	v_exp_f32_e32 v26, v26
	v_exp_f32_e32 v27, v27
	v_exp_f32_e32 v28, v28
	v_exp_f32_e32 v29, v29
	v_exp_f32_e32 v86, v18
	v_exp_f32_e32 v87, v19
	v_exp_f32_e32 v20, v20
	v_exp_f32_e32 v21, v21
	v_exp_f32_e32 v30, v30
	v_exp_f32_e32 v22, v22
	v_add_f32_e32 v18, v26, v27
	v_add_f32_e32 v19, v28, v29
	v_exp_f32_e32 v31, v31
	v_exp_f32_e32 v23, v23
	v_add_f32_e32 v18, v18, v19
	v_add_f32_e32 v19, v86, v87
	v_add_f32_e32 v82, v20, v21
	v_add_f32_e32 v19, v19, v82
	v_exp_f32_e32 v32, v32
	v_exp_f32_e32 v24, v24
	v_add_f32_e32 v18, v18, v30
	v_add_f32_e32 v19, v19, v22
	v_exp_f32_e32 v33, v33
	v_exp_f32_e32 v25, v25
	v_add_f32_e32 v18, v31, v18
	v_add_f32_e32 v19, v23, v19
	v_exp_f32_e32 v42, v42
	v_exp_f32_e32 v58, v58
	v_add_f32_e32 v18, v32, v18
	v_add_f32_e32 v19, v24, v19
	v_exp_f32_e32 v43, v43
	v_exp_f32_e32 v59, v59
	v_add_f32_e32 v18, v33, v18
	v_add_f32_e32 v19, v25, v19
	v_exp_f32_e32 v44, v44
	v_exp_f32_e32 v60, v60
	v_add_f32_e32 v18, v42, v18
	v_add_f32_e32 v19, v58, v19
	v_exp_f32_e32 v45, v45
	v_exp_f32_e32 v61, v61
	v_add_f32_e32 v18, v43, v18
	v_add_f32_e32 v19, v59, v19
	v_exp_f32_e32 v74, v74
	v_exp_f32_e32 v78, v78
	v_add_f32_e32 v18, v44, v18
	v_add_f32_e32 v19, v60, v19
	v_exp_f32_e32 v75, v75
	v_exp_f32_e32 v79, v79
	v_add_f32_e32 v18, v45, v18
	v_add_f32_e32 v19, v61, v19
	v_exp_f32_e32 v76, v76
	v_exp_f32_e32 v80, v80
	v_add_f32_e32 v18, v74, v18
	v_add_f32_e32 v19, v78, v19
	v_exp_f32_e32 v77, v77
	v_exp_f32_e32 v81, v81
	v_add_f32_e32 v18, v75, v18
	v_add_f32_e32 v19, v79, v19
	s_mov_b32 s4, 1
	v_add_f32_e32 v18, v76, v18
	v_add_f32_e32 v82, v80, v19
	v_cvt_pk_bf16_f32 v83, v28, v29
	v_add_f32_e32 v19, v77, v18
	v_add_f32_e32 v18, v81, v82
	s_waitcnt vmcnt(3) lgkmcnt(0)
	s_barrier
	s_cmp_lg_u32 s4, 0
	v_pk_add_f32 v[168:169], v[18:19], 0 op_sel_hi:[1,0]
	v_mov_b32_e32 v18, 0
	v_cvt_pk_bf16_f32 v82, v26, v27
	v_cvt_pk_bf16_f32 v84, v30, v31
	v_cvt_pk_bf16_f32 v85, v32, v33
	v_cvt_pk_bf16_f32 v94, v86, v87
	v_cvt_pk_bf16_f32 v95, v20, v21
	v_cvt_pk_bf16_f32 v96, v22, v23
	v_cvt_pk_bf16_f32 v97, v24, v25
	v_cvt_pk_bf16_f32 v98, v42, v43
	v_cvt_pk_bf16_f32 v99, v44, v45
	v_cvt_pk_bf16_f32 v100, v74, v75
	v_cvt_pk_bf16_f32 v101, v76, v77
	v_cvt_pk_bf16_f32 v102, v58, v59
	v_cvt_pk_bf16_f32 v103, v60, v61
	v_cvt_pk_bf16_f32 v104, v78, v79
	v_cvt_pk_bf16_f32 v105, v80, v81
	s_cselect_b64 s[4:5], -1, 0
	s_mov_b32 s30, 2
	v_mov_b32_e32 v19, v18
	v_mov_b32_e32 v20, v18
	v_mov_b32_e32 v21, v18
	v_mov_b32_e32 v22, v18
	v_mov_b32_e32 v23, v18
	v_mov_b32_e32 v24, v18
	v_mov_b32_e32 v25, v18
	v_mov_b32_e32 v26, v18
	v_mov_b32_e32 v27, v18
	v_mov_b32_e32 v28, v18
	v_mov_b32_e32 v29, v18
	v_mov_b32_e32 v30, v18
	v_mov_b32_e32 v31, v18
	v_mov_b32_e32 v32, v18
	v_mov_b32_e32 v33, v18
	v_mov_b32_e32 v42, v18
	v_mov_b32_e32 v43, v18
	v_mov_b32_e32 v44, v18
	v_mov_b32_e32 v45, v18
	v_mov_b32_e32 v58, v18
	v_mov_b32_e32 v59, v18
	v_mov_b32_e32 v60, v18
	v_mov_b32_e32 v61, v18
	v_mov_b32_e32 v74, v18
	v_mov_b32_e32 v75, v18
	v_mov_b32_e32 v76, v18
	v_mov_b32_e32 v77, v18
	v_mov_b32_e32 v78, v18
	v_mov_b32_e32 v79, v18
	v_mov_b32_e32 v80, v18
	v_mov_b32_e32 v81, v18
	v_mov_b32_e32 v86, v18
	v_mov_b32_e32 v87, v18
	v_mov_b32_e32 v88, v18
	v_mov_b32_e32 v89, v18
	v_mov_b32_e32 v90, v18
	v_mov_b32_e32 v91, v18
	v_mov_b32_e32 v92, v18
	v_mov_b32_e32 v93, v18
	v_mov_b32_e32 v106, v18
	v_mov_b32_e32 v107, v18
	v_mov_b32_e32 v108, v18
	v_mov_b32_e32 v109, v18
	v_mov_b32_e32 v110, v18
	v_mov_b32_e32 v111, v18
	v_mov_b32_e32 v112, v18
	v_mov_b32_e32 v113, v18
	v_mov_b32_e32 v114, v18
	v_mov_b32_e32 v115, v18
	v_mov_b32_e32 v116, v18
	v_mov_b32_e32 v117, v18
	v_mov_b32_e32 v118, v18
	v_mov_b32_e32 v119, v18
	v_mov_b32_e32 v120, v18
	v_mov_b32_e32 v121, v18
	v_mov_b32_e32 v122, v18
	v_mov_b32_e32 v123, v18
	v_mov_b32_e32 v124, v18
	v_mov_b32_e32 v125, v18
	v_mov_b32_e32 v126, v18
	v_mov_b32_e32 v127, v18
	v_mov_b32_e32 v128, v18
	v_mov_b32_e32 v129, v18
